# v_mov_b64 register-pair copies (148 sites) split into two v_mov_b32; on top of v39
# baseline (speedup 1.0000x reference)
.LBB0_87:
	s_or_b64 exec, exec, s[18:19]
	v_ashrrev_i32_e32 v5, 31, v4
	v_cmp_lt_i32_e32 vcc, -1, v4
	v_lshl_add_u64 v[24:25], v[4:5], 2, s[10:11]
	v_add_u32_e32 v3, s5, v28
	s_lshl_b32 s18, s31, 11
	v_mov_b32_e32 v4, v2
	v_mov_b32_e32 v5, v2
	v_subrev_u32_e32 v26, s18, v3
	v_mov_b32_e32 v3, v2
	v_mov_b32_e32 v8, v4
	v_mov_b32_e32 v9, v5
	s_and_b64 s[18:19], s[2:3], vcc
	v_mov_b32_e32 v6, v2
	v_mov_b32_e32 v7, v3
	s_and_saveexec_b64 s[20:21], s[18:19]
	s_cbranch_execz .LBB0_89
	v_mad_i64_i32 v[4:5], s[34:35], v26, s27, v[24:25]
	global_load_dwordx4 v[6:9], v[4:5], off

.LBB0_91:
	v_mov_b32_e32 v4, v2
	v_mov_b32_e32 v5, v2
	v_mov_b32_e32 v3, v2
	v_mov_b32_e32 v12, v4
	v_mov_b32_e32 v13, v5
	v_mov_b32_e32 v10, v2
	v_mov_b32_e32 v11, v3
	s_and_saveexec_b64 s[20:21], s[18:19]
	s_cbranch_execz .LBB0_93
	v_add_u32_e32 v3, 16, v26
	v_mad_i64_i32 v[4:5], s[34:35], v3, s27, v[24:25]
	global_load_dwordx4 v[10:13], v[4:5], off

.LBB0_95:
	v_mov_b32_e32 v4, v2
	v_mov_b32_e32 v5, v2
	v_mov_b32_e32 v3, v2
	v_mov_b32_e32 v8, v4
	v_mov_b32_e32 v9, v5
	v_mov_b32_e32 v6, v2
	v_mov_b32_e32 v7, v3
	s_and_saveexec_b64 s[20:21], s[18:19]
	s_cbranch_execz .LBB0_97
	v_add_u32_e32 v3, 32, v26
	v_mad_i64_i32 v[4:5], s[34:35], v3, s27, v[24:25]
	global_load_dwordx4 v[6:9], v[4:5], off

.LBB0_99:
	v_mov_b32_e32 v4, v2
	v_mov_b32_e32 v5, v2
	v_mov_b32_e32 v3, v2
	v_mov_b32_e32 v12, v4
	v_mov_b32_e32 v13, v5
	v_mov_b32_e32 v10, v2
	v_mov_b32_e32 v11, v3
	s_and_saveexec_b64 s[20:21], s[18:19]
	s_cbranch_execz .LBB0_101
	v_add_u32_e32 v3, 48, v26
	v_mad_i64_i32 v[4:5], s[18:19], v3, s27, v[24:25]
	global_load_dwordx4 v[10:13], v[4:5], off

.LBB0_123:
	s_cmpk_lt_i32 s93, 0x60
	v_readlane_b32 s0, v254, 8
	s_cselect_b64 s[18:19], -1, 0
	s_lshl_b32 s37, s0, 7
	v_readlane_b32 s0, v254, 9
	s_lshl_b32 s36, s0, 6
	s_cmp_lt_i32 s93, 64
	s_cselect_b64 s[16:17], -1, 0
	s_abs_i32 s0, s92
	s_waitcnt vmcnt(5)
	v_cvt_f32_u32_e32 v2, s0
	v_readlane_b32 s1, v254, 10
	s_lshl_b32 s34, s1, 7
	v_readlane_b32 s1, v254, 11
	v_rcp_iflag_f32_e32 v2, v2
	s_lshl_b32 s35, s1, 6
	s_sub_i32 s1, 0, s0
	s_waitcnt lgkmcnt(0)
	v_mul_f32_e32 v2, 0x4f7ffffe, v2
	v_cvt_u32_f32_e32 v2, v2
	s_barrier
	v_readfirstlane_b32 s2, v2
	s_mul_i32 s1, s1, s2
	s_mul_hi_u32 s1, s2, s1
	s_add_i32 s2, s2, s1
	s_mul_hi_u32 s1, s2, 0x880
	s_mul_i32 s1, s1, s0
	s_sub_i32 s1, 0x880, s1
	s_sub_i32 s2, s1, s0
	s_cmp_ge_u32 s1, s0
	s_cselect_b32 s1, s2, s1
	s_sub_i32 s2, s1, s0
	s_cmp_ge_u32 s1, s0
	s_cselect_b32 s0, s2, s1
	s_add_u32 s20, s6, 0x10000
	s_addc_u32 s21, s7, 0
	s_cmp_lg_u32 s0, 0
	v_readlane_b32 s0, v254, 5
	s_nop 1
	v_add_u32_e32 v18, s0, v32
	s_movk_i32 s0, 0x104
	v_cmp_gt_i32_e64 s[0:1], s0, v18
	s_cbranch_scc0 .LBB0_138
	s_and_saveexec_b64 s[4:5], s[0:1]
	v_readlane_b32 s28, v254, 6
	v_readlane_b32 s29, v254, 7
	s_cbranch_execz .LBB0_132
	v_cvt_f32_u32_e32 v2, s28
	v_add_u32_e32 v19, s28, v18
	s_movk_i32 s2, 0x104
	v_mov_b32_e32 v3, s28
	v_rcp_iflag_f32_e32 v2, v2
	v_cmp_gt_i32_e32 vcc, s2, v19
	s_sub_i32 s8, 0, s28
	v_max_i32_e32 v4, 0x104, v19
	v_mul_f32_e32 v2, 0x4f7ffffe, v2
	v_cvt_u32_f32_e32 v2, v2
	v_addc_co_u32_e64 v3, s[2:3], v18, v3, vcc
	v_sub_u32_e32 v3, v4, v3
	v_mul_lo_u32 v4, s8, v2
	v_mul_hi_u32 v4, v2, v4
	v_add_u32_e32 v2, v2, v4
	v_mul_hi_u32 v2, v3, v2
	v_mul_lo_u32 v4, v2, s28
	v_sub_u32_e32 v3, v3, v4
	v_add_u32_e32 v4, 1, v2
	v_cmp_le_u32_e64 s[2:3], s28, v3
	s_mov_b64 s[8:9], -1
	s_nop 0
	v_cndmask_b32_e64 v2, v2, v4, s[2:3]
	v_subrev_u32_e32 v4, s28, v3
	v_cndmask_b32_e64 v3, v3, v4, s[2:3]
	v_add_u32_e32 v4, 1, v2
	v_cmp_le_u32_e64 s[2:3], s28, v3
	s_nop 1
	v_cndmask_b32_e64 v2, v2, v4, s[2:3]
	v_addc_co_u32_e32 v4, vcc, 1, v2, vcc
	v_cmp_lt_u32_e32 vcc, 1, v4
	v_mov_b32_e32 v2, v18
	s_and_saveexec_b64 s[2:3], vcc
	s_cbranch_execz .LBB0_129
	v_and_b32_e32 v5, -2, v4
	s_lshl_b32 s10, s92, 10
	s_mov_b32 s11, s10
	s_mov_b64 s[8:9], 0
	s_mov_b32 s22, 0x7e07e07f
	s_waitcnt vmcnt(4)
	v_mov_b32_e32 v6, 0x2000
	v_mov_b32_e32 v7, v5
	v_mov_b32_e32 v2, v18
	v_mov_b32_e32 v3, v19
	s_waitcnt vmcnt(0)

.LBB0_223:
	s_and_saveexec_b64 s[2:3], s[0:1]
	v_readlane_b32 s24, v254, 6
	v_readlane_b32 s25, v254, 7
	s_cbranch_execz .LBB0_231
	s_waitcnt vmcnt(2)
	v_cvt_f32_u32_e32 v2, s24
	v_add_u32_e32 v19, s24, v18
	s_movk_i32 s0, 0x104
	v_mov_b32_e32 v3, s24
	v_rcp_iflag_f32_e32 v2, v2
	v_cmp_gt_i32_e32 vcc, s0, v19
	s_sub_i32 s4, 0, s24
	v_max_i32_e32 v4, 0x104, v19
	v_mul_f32_e32 v2, 0x4f7ffffe, v2
	v_cvt_u32_f32_e32 v2, v2
	v_addc_co_u32_e64 v3, s[0:1], v18, v3, vcc
	v_sub_u32_e32 v3, v4, v3
	v_mul_lo_u32 v4, s4, v2
	v_mul_hi_u32 v4, v2, v4
	v_add_u32_e32 v2, v2, v4
	v_mul_hi_u32 v2, v3, v2
	v_mul_lo_u32 v4, v2, s24
	v_sub_u32_e32 v3, v3, v4
	v_add_u32_e32 v4, 1, v2
	v_cmp_le_u32_e64 s[0:1], s24, v3
	s_mov_b64 s[4:5], -1
	s_nop 0
	v_cndmask_b32_e64 v2, v2, v4, s[0:1]
	v_subrev_u32_e32 v4, s24, v3
	v_cndmask_b32_e64 v3, v3, v4, s[0:1]
	v_add_u32_e32 v4, 1, v2
	v_cmp_le_u32_e64 s[0:1], s24, v3
	s_nop 1
	v_cndmask_b32_e64 v2, v2, v4, s[0:1]
	v_addc_co_u32_e32 v4, vcc, 1, v2, vcc
	v_cmp_lt_u32_e32 vcc, 1, v4
	v_mov_b32_e32 v2, v18
	s_and_saveexec_b64 s[0:1], vcc
	s_cbranch_execz .LBB0_228
	v_and_b32_e32 v5, -2, v4
	s_waitcnt lgkmcnt(0)
	s_lshl_b32 s8, s92, 10
	s_mov_b32 s9, s8
	s_mov_b64 s[4:5], 0
	s_mov_b32 s10, 0x7e07e07f
	v_mov_b32_e32 v6, 0x2000
	v_mov_b32_e32 v7, v5
	v_mov_b32_e32 v2, v18
	v_mov_b32_e32 v3, v19

.LBB0_370:
	v_mov_b32_e32 v4, v2
	v_mov_b32_e32 v5, v2
	v_mov_b32_e32 v3, v2
	v_mov_b32_e32 v12, v4
	v_mov_b32_e32 v13, v5
	v_mov_b32_e32 v10, v2
	v_mov_b32_e32 v11, v3
	s_waitcnt vmcnt(0)
	v_mul_f32_e64 v4, v8, s16
	v_mul_f32_e64 v5, v9, s16
	s_and_b64 vcc, exec, s[4:5]
	v_mul_f32_e64 v30, v6, s16
	v_mul_f32_e64 v31, v7, s16
	s_cbranch_vccnz .LBB0_372

.LBB0_386:
	v_mov_b32_e32 v4, v2
	v_mov_b32_e32 v5, v2
	v_mov_b32_e32 v3, v2
	v_mov_b32_e32 v8, v4
	v_mov_b32_e32 v9, v5
	v_mov_b32_e32 v6, v2
	v_mov_b32_e32 v7, v3
	s_and_b64 vcc, exec, s[4:5]
	s_cbranch_vccz .LBB0_377
	s_branch .LBB0_378
.LBB0_387:
	v_mov_b32_e32 v4, v2
	v_mov_b32_e32 v5, v2
	v_mov_b32_e32 v3, v2
	v_mov_b32_e32 v12, v4
	v_mov_b32_e32 v13, v5
	v_mov_b32_e32 v10, v2
	v_mov_b32_e32 v11, v3
	s_waitcnt vmcnt(0)
	v_mul_f32_e64 v16, v8, s16
	v_mul_f32_e64 v17, v9, s16
	s_and_b64 vcc, exec, s[4:5]
	v_mul_f32_e64 v24, v6, s16
	v_mul_f32_e64 v25, v7, s16
	s_cbranch_vccz .LBB0_380
	s_branch .LBB0_381
.LBB0_388:
	v_mov_b32_e32 v4, v2
	v_mov_b32_e32 v5, v2
	v_mov_b32_e32 v3, v2
	v_mov_b32_e32 v8, v4
	v_mov_b32_e32 v9, v5
	v_mov_b32_e32 v6, v2
	v_mov_b32_e32 v7, v3
	s_waitcnt vmcnt(0)
	v_mul_f32_e64 v26, v12, s16
	v_mul_f32_e64 v27, v13, s16
	s_and_b64 vcc, exec, s[4:5]
	v_mul_f32_e64 v28, v10, s16
	v_mul_f32_e64 v29, v11, s16
	s_cbranch_vccz .LBB0_383
	s_branch .LBB0_384

.LBB0_513:
	v_mov_b32_e32 v4, v2
	v_mov_b32_e32 v5, v2
	v_mov_b32_e32 v3, v2
	v_mov_b32_e32 v12, v4
	v_mov_b32_e32 v13, v5
	v_mov_b32_e32 v10, v2
	v_mov_b32_e32 v11, v3
	s_waitcnt vmcnt(0)
	v_mul_f32_e64 v4, v8, s16
	v_mul_f32_e64 v5, v9, s16
	s_and_b64 vcc, exec, s[2:3]
	v_mul_f32_e64 v24, v6, s16
	v_mul_f32_e64 v25, v7, s16
	s_cbranch_vccnz .LBB0_515

.LBB0_529:
	v_mov_b32_e32 v4, v2
	v_mov_b32_e32 v5, v2
	v_mov_b32_e32 v3, v2
	v_mov_b32_e32 v8, v4
	v_mov_b32_e32 v9, v5
	v_mov_b32_e32 v6, v2
	v_mov_b32_e32 v7, v3
	s_and_b64 vcc, exec, s[2:3]
	s_cbranch_vccz .LBB0_520
	s_branch .LBB0_521
.LBB0_530:
	v_mov_b32_e32 v4, v2
	v_mov_b32_e32 v5, v2
	v_mov_b32_e32 v3, v2
	v_mov_b32_e32 v12, v4
	v_mov_b32_e32 v13, v5
	v_mov_b32_e32 v10, v2
	v_mov_b32_e32 v11, v3
	s_waitcnt vmcnt(0)
	v_mul_f32_e64 v16, v8, s16
	v_mul_f32_e64 v17, v9, s16
	s_and_b64 vcc, exec, s[2:3]
	v_mul_f32_e64 v18, v6, s16
	v_mul_f32_e64 v19, v7, s16
	s_cbranch_vccz .LBB0_523
	s_branch .LBB0_524
.LBB0_531:
	v_mov_b32_e32 v4, v2
	v_mov_b32_e32 v5, v2
	v_mov_b32_e32 v3, v2
	v_mov_b32_e32 v8, v4
	v_mov_b32_e32 v9, v5
	v_mov_b32_e32 v6, v2
	v_mov_b32_e32 v7, v3
	s_waitcnt vmcnt(0)
	v_mul_f32_e64 v20, v12, s16
	v_mul_f32_e64 v21, v13, s16
	s_and_b64 vcc, exec, s[2:3]
	v_mul_f32_e64 v22, v10, s16
	v_mul_f32_e64 v23, v11, s16
	s_cbranch_vccz .LBB0_526
	s_branch .LBB0_527

.LBB0_804:
	s_bfe_u32 s0, s66, 0x20001
	s_bfe_u32 s1, s78, 0x10007
	s_lshl_b32 s12, s1, 8
	s_lshl_b32 s44, s0, 9
	s_or_b32 s48, s44, s12
	s_mulk_i32 s0, 0x180
	s_mul_i32 s12, s1, 0xc0
	s_add_i32 s0, s0, s12
	s_lshl_b32 s50, s0, 1
	s_ashr_i32 s0, s78, 4
	s_lshl_b32 s12, s78, 1
	s_and_b32 s0, s0, -16
	s_and_b32 s44, s12, 8
	s_bfe_u32 s80, s78, 0x40003
	s_or_b32 s0, s0, s44
	s_xor_b32 s49, s80, 31
	s_ashr_i32 s0, s0, 3
	s_and_b32 s12, s12, 6
	s_lshl_b32 s83, s49, 8
	s_or_b32 s46, s12, s1
	s_ashr_i32 s1, s0, 31
	s_add_i32 s84, s83, s63
	s_lshr_b32 s81, s78, 3
	v_mov_b32_e32 v172, v1
	s_lshl_b64 s[52:53], s[0:1], 13
	s_ashr_i32 s12, s84, 31
	s_add_u32 s54, s52, s84
	v_and_b32_e32 v168, 31, v172
	v_or_b32_e32 v38, s54, v168
	s_addc_u32 s55, s53, s12
	v_mad_u64_u32 v[2:3], s[44:45], v38, s68, v[146:147]
	s_mul_i32 s82, s46, 0xc0
	v_bfe_u32 v173, v172, 5, 1
	v_mad_i32_i24 v3, s55, v162, v3
	s_lshl_b32 s12, s82, 1
	v_lshl_add_u64 v[2:3], v[2:3], 0, s[12:13]
	v_lshlrev_b32_e32 v148, 4, v173
	v_lshl_add_u64 v[40:41], v[2:3], 0, v[148:149]
	global_load_dwordx4 v[6:9], v[40:41], off
	global_load_dwordx4 v[14:17], v[40:41], off offset:32
	global_load_dwordx4 v[30:33], v[40:41], off offset:64
	global_load_dwordx4 v[34:37], v[40:41], off offset:96
	global_load_dwordx4 v[50:53], v[40:41], off offset:128
	global_load_dwordx4 v[26:29], v[40:41], off offset:160
	global_load_dwordx4 v[22:25], v[40:41], off offset:192
	global_load_dwordx4 v[18:21], v[40:41], off offset:224
	global_load_dwordx4 v[10:13], v[40:41], off offset:256
	global_load_dwordx4 v[42:45], v[40:41], off offset:288
	s_waitcnt lgkmcnt(0)
	global_load_dwordx4 v[2:5], v[40:41], off offset:320
	global_load_dwordx4 v[46:49], v[40:41], off offset:352
	v_and_b32_e32 v40, 32, v172
	v_mov_b32_e32 v39, s55
	s_mul_i32 s86, s0, 0x1800000
	s_mul_hi_i32 s51, s0, 0x1800000
	s_add_u32 s44, s33, s86
	s_addc_u32 s45, s58, s51
	s_lshl_b64 s[56:57], s[0:1], 24
	s_lshl_b32 s79, s46, 7
	s_add_u32 s44, s44, s12
	s_addc_u32 s45, s45, 0
	s_mov_b32 m0, s71
	s_add_u32 s0, s59, s56
	s_addc_u32 s1, s60, s57
	s_lshl_b32 s12, s46, 8
	s_add_u32 s46, s0, s12
	s_addc_u32 s47, s1, 0
	s_lshl_b32 s85, s49, 2
	s_add_i32 s85, s85, 4
	s_or_b32 s48, s56, s48
	s_add_u32 s48, s48, 0x29020000
	s_addc_u32 s49, s57, 0
	s_or_b32 s50, s86, s50
	s_add_u32 s50, s50, 0x23030000
	s_addc_u32 s51, s51, 0
	s_mov_b32 s12, 1
	s_movk_i32 s86, 0xff00
	s_waitcnt vmcnt(0)
	v_lshlrev_b32_e32 v227, 16, v26
	v_lshlrev_b32_e32 v177, 16, v6
	v_and_b32_e32 v174, 0xffff0000, v6
	v_lshlrev_b32_e32 v170, 16, v7
	v_and_b32_e32 v167, 0xffff0000, v7
	v_lshlrev_b32_e32 v180, 16, v8
	v_and_b32_e32 v176, 0xffff0000, v8
	v_lshlrev_b32_e32 v171, 16, v9
	v_and_b32_e32 v169, 0xffff0000, v9
	v_lshlrev_b32_e32 v185, 16, v14
	v_and_b32_e32 v182, 0xffff0000, v14
	v_lshlrev_b32_e32 v179, 16, v15
	v_and_b32_e32 v175, 0xffff0000, v15
	v_lshlrev_b32_e32 v187, 16, v16
	v_and_b32_e32 v183, 0xffff0000, v16
	v_lshlrev_b32_e32 v181, 16, v17
	v_and_b32_e32 v178, 0xffff0000, v17
	v_lshlrev_b32_e32 v201, 16, v34
	v_and_b32_e32 v198, 0xffff0000, v34
	v_lshlrev_b32_e32 v196, 16, v35
	v_and_b32_e32 v192, 0xffff0000, v35
	v_lshlrev_b32_e32 v202, 16, v36
	v_and_b32_e32 v199, 0xffff0000, v36
	v_lshlrev_b32_e32 v197, 16, v37
	v_and_b32_e32 v194, 0xffff0000, v37
	v_and_b32_e32 v228, 0xffff0000, v26
	global_load_dwordx4 v[142:145], v40, s[4:5] offset:704
	global_load_dwordx4 v[130:133], v40, s[4:5] offset:720
	global_load_dwordx4 v[6:9], v40, s[4:5] offset:592
	v_lshlrev_b32_e32 v229, 16, v27
	global_load_dwordx4 v[14:17], v40, s[4:5] offset:576
	v_and_b32_e32 v230, 0xffff0000, v27
	v_lshlrev_b32_e32 v231, 16, v28
	v_and_b32_e32 v232, 0xffff0000, v28
	v_lshlrev_b32_e32 v233, 16, v29
	v_and_b32_e32 v234, 0xffff0000, v29
	global_load_dwordx4 v[34:37], v40, s[4:5] offset:640
	global_load_dwordx4 v[156:159], v40, s[4:5] offset:656
	global_load_dwordx4 v[26:29], v40, s[4:5] offset:528
	v_mul_f32_e32 v209, v174, v174
	v_fmac_f32_e32 v209, v177, v177
	v_fmac_f32_e32 v209, v170, v170
	v_fmac_f32_e32 v209, v167, v167
	v_fmac_f32_e32 v209, v180, v180
	v_fmac_f32_e32 v209, v176, v176
	v_fmac_f32_e32 v209, v171, v171
	v_fmac_f32_e32 v209, v169, v169
	v_fmac_f32_e32 v209, v185, v185
	v_lshlrev_b32_e32 v193, 16, v30
	v_and_b32_e32 v190, 0xffff0000, v30
	v_lshlrev_b32_e32 v188, 16, v31
	v_and_b32_e32 v184, 0xffff0000, v31
	v_lshlrev_b32_e32 v195, 16, v32
	v_and_b32_e32 v191, 0xffff0000, v32
	v_lshlrev_b32_e32 v189, 16, v33
	v_and_b32_e32 v186, 0xffff0000, v33
	v_fmac_f32_e32 v209, v182, v182
	global_load_dwordx4 v[30:33], v40, s[4:5] offset:512
	v_fmac_f32_e32 v209, v179, v179
	v_fmac_f32_e32 v209, v175, v175
	v_fmac_f32_e32 v209, v187, v187
	v_fmac_f32_e32 v209, v183, v183
	v_fmac_f32_e32 v209, v181, v181
	v_fmac_f32_e32 v209, v178, v178
	v_fmac_f32_e32 v209, v193, v193
	v_fmac_f32_e32 v209, v190, v190
	v_fmac_f32_e32 v209, v188, v188
	v_fmac_f32_e32 v209, v184, v184
	v_fmac_f32_e32 v209, v195, v195
	v_fmac_f32_e32 v209, v191, v191
	v_fmac_f32_e32 v209, v189, v189
	v_fmac_f32_e32 v209, v186, v186
	v_fmac_f32_e32 v209, v201, v201
	v_fmac_f32_e32 v209, v198, v198
	v_fmac_f32_e32 v209, v196, v196
	v_fmac_f32_e32 v209, v192, v192
	v_fmac_f32_e32 v209, v202, v202
	v_fmac_f32_e32 v209, v199, v199
	v_fmac_f32_e32 v209, v197, v197
	v_lshlrev_b32_e32 v207, 16, v50
	v_fmac_f32_e32 v209, v194, v194
	v_and_b32_e32 v205, 0xffff0000, v50
	v_fmac_f32_e32 v209, v207, v207
	v_lshlrev_b32_e32 v203, 16, v51
	v_fmac_f32_e32 v209, v205, v205
	v_and_b32_e32 v200, 0xffff0000, v51
	v_fmac_f32_e32 v209, v203, v203
	v_lshlrev_b32_e32 v208, 16, v52
	v_fmac_f32_e32 v209, v200, v200
	v_and_b32_e32 v206, 0xffff0000, v52
	v_fmac_f32_e32 v209, v208, v208
	v_lshlrev_b32_e32 v204, 16, v53
	v_fmac_f32_e32 v209, v206, v206
	v_and_b32_e32 v226, 0xffff0000, v53
	v_fmac_f32_e32 v209, v204, v204
	v_fmac_f32_e32 v209, v226, v226
	v_fmac_f32_e32 v209, v227, v227
	v_fmac_f32_e32 v209, v228, v228
	v_fmac_f32_e32 v209, v229, v229
	v_fmac_f32_e32 v209, v230, v230
	global_load_dwordx4 v[110:113], v40, s[4:5] offset:16
	global_load_dwordx4 v[114:117], v40, s[4:5]
	global_load_dwordx4 v[102:105], v40, s[4:5] offset:80
	global_load_dwordx4 v[106:109], v40, s[4:5] offset:64
	global_load_dwordx4 v[94:97], v40, s[4:5] offset:144
	global_load_dwordx4 v[98:101], v40, s[4:5] offset:128
	global_load_dwordx4 v[86:89], v40, s[4:5] offset:208
	global_load_dwordx4 v[90:93], v40, s[4:5] offset:192
	global_load_dwordx4 v[78:81], v40, s[4:5] offset:272
	global_load_dwordx4 v[82:85], v40, s[4:5] offset:256
	global_load_dwordx4 v[70:73], v40, s[4:5] offset:336
	global_load_dwordx4 v[74:77], v40, s[4:5] offset:320
	global_load_dwordx4 v[62:65], v40, s[4:5] offset:400
	global_load_dwordx4 v[66:69], v40, s[4:5] offset:384
	global_load_dwordx4 v[54:57], v40, s[4:5] offset:464
	global_load_dwordx4 v[58:61], v40, s[4:5] offset:448
	v_fmac_f32_e32 v209, v231, v231
	v_fmac_f32_e32 v209, v232, v232
	v_fmac_f32_e32 v209, v233, v233
	v_fmac_f32_e32 v209, v234, v234
	s_waitcnt vmcnt(29)
	v_lshlrev_b32_e32 v235, 16, v22
	v_and_b32_e32 v236, 0xffff0000, v22
	v_fmac_f32_e32 v209, v235, v235
	v_lshlrev_b32_e32 v237, 16, v23
	v_fmac_f32_e32 v209, v236, v236
	v_and_b32_e32 v238, 0xffff0000, v23
	v_fmac_f32_e32 v209, v237, v237
	v_lshlrev_b32_e32 v239, 16, v24
	v_fmac_f32_e32 v209, v238, v238
	v_and_b32_e32 v240, 0xffff0000, v24
	v_fmac_f32_e32 v209, v239, v239
	v_lshlrev_b32_e32 v241, 16, v25
	v_fmac_f32_e32 v209, v240, v240
	v_and_b32_e32 v242, 0xffff0000, v25
	v_fmac_f32_e32 v209, v241, v241
	v_fmac_f32_e32 v209, v242, v242
	s_waitcnt vmcnt(28)
	v_lshlrev_b32_e32 v243, 16, v18
	v_and_b32_e32 v244, 0xffff0000, v18
	v_fmac_f32_e32 v209, v243, v243
	v_lshlrev_b32_e32 v245, 16, v19
	v_fmac_f32_e32 v209, v244, v244
	v_and_b32_e32 v246, 0xffff0000, v19
	v_fmac_f32_e32 v209, v245, v245
	v_lshlrev_b32_e32 v247, 16, v20
	v_fmac_f32_e32 v209, v246, v246
	v_and_b32_e32 v248, 0xffff0000, v20
	v_fmac_f32_e32 v209, v247, v247
	v_lshlrev_b32_e32 v249, 16, v21
	v_fmac_f32_e32 v209, v248, v248
	v_and_b32_e32 v250, 0xffff0000, v21
	v_fmac_f32_e32 v209, v249, v249
	s_waitcnt vmcnt(27)
	v_lshlrev_b32_e32 v223, 16, v10
	s_waitcnt vmcnt(25)
	v_lshlrev_b32_e32 v222, 16, v2
	v_fmac_f32_e32 v209, v250, v250
	s_waitcnt vmcnt(18)
	v_mov_b32_e32 v150, v158
	v_mov_b32_e32 v158, v156
	v_lshlrev_b32_e32 v156, 16, v3
	v_and_b32_e32 v160, 0xffff0000, v3
	v_and_b32_e32 v225, 0xffff0000, v10
	v_and_b32_e32 v224, 0xffff0000, v2
	v_mul_f32_e32 v2, v222, v222
	v_mul_f32_e32 v3, v223, v223
	v_mov_b32_e32 v134, v144
	v_mov_b32_e32 v140, v142
	v_lshlrev_b32_e32 v142, 16, v5
	s_waitcnt vmcnt(17)
	v_mov_b32_e32 v151, v28
	v_and_b32_e32 v144, 0xffff0000, v5
	v_mov_b32_e32 v28, v159
	v_lshlrev_b32_e32 v152, 16, v4
	v_mov_b32_e32 v159, v26
	v_and_b32_e32 v154, 0xffff0000, v4
	v_mov_b32_e32 v26, v157
	v_lshlrev_b32_e32 v157, 16, v11
	v_add_f32_e32 v3, v3, v209
	v_mul_f32_e32 v4, v224, v224
	v_mul_f32_e32 v5, v225, v225
	v_lshlrev_b32_e32 v119, 16, v45
	v_and_b32_e32 v121, 0xffff0000, v45
	v_lshlrev_b32_e32 v125, 16, v44
	v_and_b32_e32 v127, 0xffff0000, v44
	v_mul_f32_e32 v44, v156, v156
	v_mul_f32_e32 v45, v157, v157
	v_and_b32_e32 v161, 0xffff0000, v11
	v_add_f32_e32 v3, v5, v3
	v_mov_b32_e32 v122, v132
	v_mov_b32_e32 v128, v130
	v_lshlrev_b32_e32 v130, 16, v47
	v_and_b32_e32 v132, 0xffff0000, v47
	v_lshlrev_b32_e32 v136, 16, v46
	v_and_b32_e32 v138, 0xffff0000, v46
	v_lshlrev_b32_e32 v153, 16, v12
	v_mul_f32_e32 v46, v160, v160
	v_mul_f32_e32 v47, v161, v161
	v_add_f32_e32 v3, v45, v3
	v_mov_b32_e32 v123, v8
	v_mov_b32_e32 v8, v133
	v_mov_b32_e32 v129, v6
	v_mov_b32_e32 v6, v131
	v_lshlrev_b32_e32 v131, 16, v43
	v_and_b32_e32 v133, 0xffff0000, v43
	v_lshlrev_b32_e32 v137, 16, v42
	v_and_b32_e32 v139, 0xffff0000, v42
	v_mul_f32_e32 v42, v152, v152
	v_mul_f32_e32 v43, v153, v153
	v_and_b32_e32 v155, 0xffff0000, v12
	v_add_f32_e32 v3, v47, v3
	v_mov_b32_e32 v141, v14
	v_mov_b32_e32 v14, v143
	v_lshlrev_b32_e32 v143, 16, v13
	v_mul_f32_e32 v220, v154, v154
	v_mul_f32_e32 v221, v155, v155
	v_add_f32_e32 v3, v43, v3
	v_mov_b32_e32 v135, v16
	v_mov_b32_e32 v16, v145
	v_mul_f32_e32 v216, v142, v142
	v_mul_f32_e32 v217, v143, v143
	v_and_b32_e32 v145, 0xffff0000, v13
	v_add_f32_e32 v3, v221, v3
	v_mul_f32_e32 v218, v144, v144
	v_mul_f32_e32 v219, v145, v145
	v_add_f32_e32 v3, v217, v3
	v_mul_f32_e32 v212, v136, v136
	v_mul_f32_e32 v213, v137, v137
	v_add_f32_e32 v3, v219, v3
	v_mul_f32_e32 v214, v138, v138
	v_mul_f32_e32 v215, v139, v139
	v_add_f32_e32 v3, v213, v3
	v_add_f32_e32 v3, v215, v3
	v_fmac_f32_e32 v3, v131, v131
	v_fmac_f32_e32 v3, v133, v133
	v_fmac_f32_e32 v3, v125, v125
	v_fmac_f32_e32 v3, v127, v127
	v_fmac_f32_e32 v3, v119, v119
	v_fmac_f32_e32 v3, v121, v121
	v_add_f32_e32 v2, v2, v3
	v_add_f32_e32 v43, v4, v2
	v_add_f32_e32 v43, v44, v43
	v_add_f32_e32 v43, v46, v43
	v_add_f32_e32 v209, v42, v43
	v_add_f32_e32 v209, v220, v209
	v_add_f32_e32 v209, v216, v209
	v_add_f32_e32 v209, v218, v209
	v_mov_b32_e32 v218, v132
	v_mov_b32_e32 v219, v130
	v_add_f32_e32 v209, v212, v209
	v_lshlrev_b64 v[18:19], 8, v[38:39]
	v_lshlrev_b32_e32 v124, 16, v48
	v_and_b32_e32 v126, 0xffff0000, v48
	v_mul_f32_e32 v218, v218, v218
	v_mul_f32_e32 v219, v219, v219
	s_waitcnt vmcnt(16)
	v_mov_b32_e32 v213, v32
	v_add_f32_e32 v32, v214, v209
	v_lshl_add_u64 v[18:19], s[10:11], 0, v[18:19]
	v_lshlrev_b32_e32 v20, 6, v173
	v_mov_b32_e32 v21, v149
	v_mov_b32_e32 v216, v126
	v_mov_b32_e32 v217, v124
	v_add_f32_e32 v32, v219, v32
	v_lshl_add_u64 v[210:211], v[18:19], 0, v[20:21]
	v_lshlrev_b32_e32 v118, 16, v49
	v_and_b32_e32 v120, 0xffff0000, v49
	v_mul_f32_e32 v216, v216, v216
	v_mul_f32_e32 v217, v217, v217
	v_add_f32_e32 v32, v218, v32
	global_load_dwordx4 v[18:21], v[210:211], off offset:48
	global_load_dwordx4 v[22:25], v[210:211], off offset:32
	global_load_dwordx4 v[38:41], v[210:211], off offset:16
	global_load_dwordx4 v[50:53], v[210:211], off
	global_load_dwordx4 v[2:5], v[210:211], off offset:176
	global_load_dwordx4 v[10:13], v[210:211], off offset:160
	global_load_dwordx4 v[42:45], v[210:211], off offset:144
	global_load_dwordx4 v[46:49], v[210:211], off offset:128
	v_mov_b32_e32 v210, v120
	v_mov_b32_e32 v211, v118
	v_add_f32_e32 v32, v217, v32
	v_mul_f32_e32 v210, v210, v210
	v_mul_f32_e32 v211, v211, v211
	v_add_f32_e32 v32, v216, v32
	v_add_f32_e32 v32, v211, v32
	v_add_f32_e32 v32, v210, v32
	v_mov_b32_e32 v212, v36
	v_mov_b32_e32 v36, v32
	s_nop 1
	v_permlane32_swap_b32_e32 v32, v36
	v_add_f32_e32 v32, v32, v36
	v_fmamk_f32 v32, v32, 0x3baaaaab, v163
	v_mul_f32_e32 v36, 0x4b800000, v32
	v_cmp_gt_f32_e32 vcc, s69, v32
	s_nop 1
	v_cndmask_b32_e32 v32, v32, v36, vcc
	v_rsq_f32_e32 v209, v32
	v_mov_b32_e32 v32, v37
	v_mov_b32_e32 v37, v30
	v_mov_b32_e32 v36, v34
	v_mul_f32_e32 v30, 0x45800000, v209
	v_cndmask_b32_e32 v30, v209, v30, vcc
	v_mul_f32_e32 v34, 0x3dd53b94, v30
	s_waitcnt vmcnt(22)
	v_mul_f32_e32 v30, v114, v34
	v_mul_f32_e32 v114, v30, v177
	v_mul_f32_e32 v30, v110, v34
	v_mul_f32_e32 v110, v30, v180
	v_mul_f32_e32 v30, v115, v34
	v_mul_f32_e32 v115, v30, v174
	v_mul_f32_e32 v30, v111, v34
	v_mul_f32_e32 v111, v30, v176
	v_mul_f32_e32 v30, v116, v34
	v_mul_f32_e32 v116, v30, v170
	v_mul_f32_e32 v30, v112, v34
	v_mul_f32_e32 v112, v30, v171
	v_mul_f32_e32 v30, v117, v34
	v_mul_f32_e32 v117, v30, v167
	v_mul_f32_e32 v30, v113, v34
	v_mul_f32_e32 v113, v30, v169
	s_waitcnt vmcnt(20)
	v_mul_f32_e32 v30, v106, v34
	v_mul_f32_e32 v106, v30, v185
	v_mul_f32_e32 v30, v102, v34
	v_mul_f32_e32 v167, v30, v187
	v_mul_f32_e32 v30, v107, v34
	v_mul_f32_e32 v102, v30, v182
	v_mul_f32_e32 v30, v103, v34
	v_mul_f32_e32 v107, v30, v183
	v_mul_f32_e32 v30, v108, v34
	v_mul_f32_e32 v103, v30, v179
	v_mul_f32_e32 v30, v104, v34
	v_mul_f32_e32 v108, v30, v181
	v_mul_f32_e32 v30, v109, v34
	v_mul_f32_e32 v104, v30, v175
	v_mul_f32_e32 v30, v105, v34
	v_mul_f32_e32 v105, v30, v178
	s_waitcnt vmcnt(18)
	v_mul_f32_e32 v30, v98, v34
	v_mul_f32_e32 v109, v30, v193
	v_mul_f32_e32 v30, v94, v34
	v_mul_f32_e32 v94, v30, v195
	v_mul_f32_e32 v30, v99, v34
	v_mul_f32_e32 v169, v30, v190
	v_mul_f32_e32 v30, v95, v34
	v_mul_f32_e32 v95, v30, v191
	v_mul_f32_e32 v30, v100, v34
	v_mul_f32_e32 v170, v30, v188
	v_mul_f32_e32 v30, v96, v34
	v_mul_f32_e32 v96, v30, v189
	v_mul_f32_e32 v30, v101, v34
	v_mul_f32_e32 v171, v30, v184
	v_mul_f32_e32 v30, v97, v34
	v_mul_f32_e32 v97, v30, v186
	s_waitcnt vmcnt(16)
	v_mul_f32_e32 v30, v90, v34
	v_mul_f32_e32 v90, v30, v201
	v_mul_f32_e32 v30, v86, v34
	v_mul_f32_e32 v86, v30, v202
	v_mul_f32_e32 v30, v91, v34
	v_mul_f32_e32 v91, v30, v198
	v_mul_f32_e32 v30, v87, v34
	v_mul_f32_e32 v87, v30, v199
	v_mul_f32_e32 v30, v92, v34
	v_mul_f32_e32 v92, v30, v196
	v_mul_f32_e32 v30, v88, v34
	v_mul_f32_e32 v88, v30, v197
	v_mul_f32_e32 v30, v93, v34
	v_mul_f32_e32 v93, v30, v192
	v_mul_f32_e32 v30, v89, v34
	v_mul_f32_e32 v89, v30, v194
	s_waitcnt vmcnt(14)
	v_mul_f32_e32 v30, v82, v34
	v_mul_f32_e32 v82, v30, v207
	v_mul_f32_e32 v30, v34, v78
	v_mul_f32_e32 v78, v30, v208
	v_mul_f32_e32 v30, v83, v34
	v_mul_f32_e32 v83, v30, v205
	v_mul_f32_e32 v30, v34, v79
	v_mul_f32_e32 v79, v30, v206
	v_mul_f32_e32 v30, v84, v34
	v_mul_f32_e32 v84, v30, v203
	v_mul_f32_e32 v30, v34, v80
	v_mul_f32_e32 v80, v30, v204
	v_mul_f32_e32 v30, v85, v34
	v_mul_f32_e32 v85, v30, v200
	v_mul_f32_e32 v30, v34, v81
	v_mul_f32_e32 v81, v30, v226
	s_waitcnt vmcnt(12)
	v_mul_f32_e32 v30, v34, v74
	v_mul_f32_e32 v74, v30, v227
	v_mul_f32_e32 v30, v34, v70
	v_mul_f32_e32 v70, v30, v231
	v_mul_f32_e32 v30, v34, v75
	v_mul_f32_e32 v75, v30, v228
	v_mul_f32_e32 v30, v34, v71
	v_mul_f32_e32 v71, v30, v232
	v_mul_f32_e32 v30, v34, v76
	v_mul_f32_e32 v76, v30, v229
	v_mul_f32_e32 v30, v34, v72
	v_mul_f32_e32 v72, v30, v233
	v_mul_f32_e32 v30, v34, v77
	v_mul_f32_e32 v77, v30, v230
	v_mul_f32_e32 v30, v34, v73
	v_mul_f32_e32 v73, v30, v234
	s_waitcnt vmcnt(10)
	v_mul_f32_e32 v30, v34, v66
	v_mul_f32_e32 v174, v30, v235
	v_mul_f32_e32 v30, v34, v62
	v_mul_f32_e32 v175, v30, v239
	v_mul_f32_e32 v30, v34, v67
	v_mul_f32_e32 v176, v30, v236
	v_mul_f32_e32 v30, v34, v63
	v_mul_f32_e32 v177, v30, v240
	v_mul_f32_e32 v30, v34, v68
	v_mul_f32_e32 v68, v30, v237
	v_mul_f32_e32 v30, v34, v64
	v_mul_f32_e32 v178, v30, v241
	v_mul_f32_e32 v30, v34, v69
	v_mul_f32_e32 v69, v30, v238
	v_mul_f32_e32 v30, v34, v65
	v_mul_f32_e32 v179, v30, v242
	s_waitcnt vmcnt(8)
	v_mul_f32_e32 v30, v34, v58
	v_mul_f32_e32 v180, v30, v243
	v_mul_f32_e32 v30, v34, v54
	v_mul_f32_e32 v181, v30, v247
	v_mul_f32_e32 v30, v34, v59
	v_mul_f32_e32 v182, v30, v244
	v_mul_f32_e32 v30, v34, v55
	v_mul_f32_e32 v183, v30, v248
	v_mul_f32_e32 v30, v34, v60
	v_mul_f32_e32 v184, v30, v245
	v_mul_f32_e32 v30, v34, v56
	v_mul_f32_e32 v185, v30, v249
	v_mul_f32_e32 v30, v34, v61
	v_mul_f32_e32 v186, v30, v246
	v_mul_f32_e32 v30, v34, v57
	v_mul_f32_e32 v36, v34, v36
	v_mul_f32_e32 v37, v34, v37
	v_mul_f32_e32 v187, v30, v250
	v_mul_f32_e32 v36, v36, v222
	v_mul_f32_e32 v37, v37, v223
	v_mov_b32_e32 v30, v35
	v_mul_f32_e32 v54, v34, v158
	v_mul_f32_e32 v55, v34, v159
	v_mul_f32_e32 v30, v34, v30
	v_mul_f32_e32 v31, v34, v31
	v_mul_f32_e32 v26, v34, v26
	v_mul_f32_e32 v27, v34, v27
	v_mul_f32_e32 v56, v34, v212
	v_mul_f32_e32 v57, v34, v213
	v_mul_f32_e32 v58, v34, v150
	v_mul_f32_e32 v59, v34, v151
	v_mul_f32_e32 v32, v34, v32
	v_mul_f32_e32 v33, v34, v33
	v_mul_f32_e32 v28, v34, v28
	v_mul_f32_e32 v29, v34, v29
	v_mul_f32_e32 v60, v34, v140
	v_mul_f32_e32 v61, v34, v141
	v_mul_f32_e32 v62, v34, v128
	v_mul_f32_e32 v63, v34, v129
	v_mul_f32_e32 v14, v34, v14
	v_mul_f32_e32 v15, v34, v15
	v_mul_f32_e32 v6, v34, v6
	v_mul_f32_e32 v7, v34, v7
	v_mul_f32_e32 v64, v34, v134
	v_mul_f32_e32 v65, v34, v135
	v_mul_f32_e32 v66, v34, v122
	v_mul_f32_e32 v67, v34, v123
	v_mul_f32_e32 v16, v34, v16
	v_mul_f32_e32 v17, v34, v17
	v_mul_f32_e32 v8, v34, v8
	v_mul_f32_e32 v9, v34, v9
	s_waitcnt vmcnt(4)
	v_mul_f32_e32 v34, v37, v50
	v_mul_f32_e32 v35, v36, v51
	v_mul_f32_e32 v30, v30, v224
	v_mul_f32_e32 v31, v31, v225
	v_mul_f32_e32 v64, v64, v130
	v_mul_f32_e32 v65, v65, v131
	v_sub_f32_e32 v130, v34, v35
	v_mul_f32_e32 v34, v36, v50
	v_mul_f32_e32 v35, v37, v51
	v_mul_f32_e32 v56, v56, v156
	v_mul_f32_e32 v57, v57, v157
	v_add_f32_e32 v36, v35, v34
	v_mul_f32_e32 v34, v31, v52
	v_mul_f32_e32 v35, v30, v53
	v_mul_f32_e32 v30, v30, v52
	v_mul_f32_e32 v31, v31, v53
	v_sub_f32_e32 v34, v34, v35
	v_add_f32_e32 v35, v31, v30
	v_mul_f32_e32 v30, v57, v38
	v_mul_f32_e32 v31, v56, v39
	v_mul_f32_e32 v32, v32, v160
	v_mul_f32_e32 v33, v33, v161
	v_sub_f32_e32 v37, v30, v31
	v_mul_f32_e32 v30, v56, v38
	v_mul_f32_e32 v31, v57, v39
	v_mul_f32_e32 v54, v54, v152
	v_mul_f32_e32 v55, v55, v153
	v_add_f32_e32 v38, v31, v30
	v_mul_f32_e32 v30, v33, v40
	v_mul_f32_e32 v31, v32, v41
	v_sub_f32_e32 v39, v30, v31
	v_mul_f32_e32 v30, v32, v40
	v_mul_f32_e32 v31, v33, v41
	v_mul_f32_e32 v26, v26, v154
	v_mul_f32_e32 v27, v27, v155
	v_add_f32_e32 v32, v31, v30
	v_mul_f32_e32 v30, v55, v22
	v_mul_f32_e32 v31, v54, v23
	v_mul_f32_e32 v22, v54, v22
	v_mul_f32_e32 v23, v55, v23
	v_sub_f32_e32 v30, v30, v31
	v_add_f32_e32 v31, v23, v22
	v_mul_f32_e32 v22, v27, v24
	v_mul_f32_e32 v23, v26, v25
	v_mul_f32_e32 v58, v58, v142
	v_mul_f32_e32 v59, v59, v143
	v_sub_f32_e32 v33, v22, v23
	v_mul_f32_e32 v22, v26, v24
	v_mul_f32_e32 v23, v27, v25
	v_mul_f32_e32 v28, v28, v144
	v_mul_f32_e32 v29, v29, v145
	v_add_f32_e32 v24, v23, v22
	v_mul_f32_e32 v22, v59, v18
	v_mul_f32_e32 v23, v58, v19
	v_mul_f32_e32 v18, v58, v18
	v_mul_f32_e32 v19, v59, v19
	v_sub_f32_e32 v22, v22, v23
	v_add_f32_e32 v23, v19, v18
	v_mul_f32_e32 v18, v29, v20
	v_mul_f32_e32 v19, v28, v21
	v_mul_f32_e32 v60, v60, v136
	v_mul_f32_e32 v61, v61, v137
	v_sub_f32_e32 v25, v18, v19
	v_mul_f32_e32 v18, v28, v20
	v_mul_f32_e32 v19, v29, v21
	v_mul_f32_e32 v14, v14, v138
	v_mul_f32_e32 v15, v15, v139
	v_add_f32_e32 v20, v19, v18
	s_waitcnt vmcnt(0)
	v_mul_f32_e32 v18, v61, v46
	v_mul_f32_e32 v19, v60, v47
	v_sub_f32_e32 v21, v18, v19
	v_mul_f32_e32 v18, v60, v46
	v_mul_f32_e32 v19, v61, v47
	v_mul_f32_e32 v16, v16, v132
	v_mul_f32_e32 v17, v17, v133
	v_add_f32_e32 v26, v19, v18
	v_mul_f32_e32 v18, v15, v48
	v_mul_f32_e32 v19, v14, v49
	v_mul_f32_e32 v14, v14, v48
	v_mul_f32_e32 v15, v15, v49
	v_sub_f32_e32 v18, v18, v19
	v_add_f32_e32 v19, v15, v14
	v_mul_f32_e32 v14, v65, v42
	v_mul_f32_e32 v15, v64, v43
	v_sub_f32_e32 v27, v14, v15
	v_mul_f32_e32 v14, v64, v42
	v_mul_f32_e32 v15, v65, v43
	v_mul_f32_e32 v62, v62, v124
	v_mul_f32_e32 v63, v63, v125
	v_add_f32_e32 v28, v15, v14
	v_mul_f32_e32 v14, v17, v44
	v_mul_f32_e32 v15, v16, v45
	v_sub_f32_e32 v29, v14, v15
	v_mul_f32_e32 v14, v16, v44
	v_mul_f32_e32 v15, v17, v45
	v_mul_f32_e32 v6, v6, v126
	v_mul_f32_e32 v7, v7, v127
	v_add_f32_e32 v16, v15, v14
	v_mul_f32_e32 v14, v63, v10
	v_mul_f32_e32 v15, v62, v11
	v_mul_f32_e32 v10, v62, v10
	v_mul_f32_e32 v11, v63, v11
	v_mul_f32_e32 v66, v66, v118
	v_mul_f32_e32 v67, v67, v119
	v_sub_f32_e32 v14, v14, v15
	v_add_f32_e32 v15, v11, v10
	v_mul_f32_e32 v10, v7, v12
	v_mul_f32_e32 v11, v6, v13
	v_mul_f32_e32 v6, v6, v12
	v_mul_f32_e32 v7, v7, v13
	v_mul_f32_e32 v8, v8, v120
	v_mul_f32_e32 v9, v9, v121
	v_sub_f32_e32 v10, v10, v11
	v_add_f32_e32 v11, v7, v6
	v_mul_f32_e32 v6, v67, v2
	v_mul_f32_e32 v7, v66, v3
	v_mul_f32_e32 v2, v66, v2
	v_mul_f32_e32 v3, v67, v3
	v_sub_f32_e32 v6, v6, v7
	v_add_f32_e32 v7, v3, v2
	v_mul_f32_e32 v2, v9, v4
	v_mul_f32_e32 v3, v8, v5
	v_sub_f32_e32 v12, v2, v3
	v_mul_f32_e32 v2, v8, v4
	v_mul_f32_e32 v3, v9, v5
	v_cvt_pk_bf16_f32 v98, v114, v115
	v_cvt_pk_bf16_f32 v99, v116, v117
	v_cvt_pk_bf16_f32 v100, v110, v111
	v_cvt_pk_bf16_f32 v101, v112, v113
	v_cvt_pk_bf16_f32 v102, v106, v102
	s_nop 0
	v_add_f32_e32 v2, v3, v2
	v_cvt_pk_bf16_f32 v103, v103, v104
	v_cvt_pk_bf16_f32 v104, v167, v107
	v_cvt_pk_bf16_f32 v105, v108, v105
	v_cvt_pk_bf16_f32 v106, v109, v169
	v_cvt_pk_bf16_f32 v107, v170, v171
	v_cvt_pk_bf16_f32 v108, v94, v95
	v_cvt_pk_bf16_f32 v109, v96, v97
	v_cvt_pk_bf16_f32 v110, v90, v91
	v_cvt_pk_bf16_f32 v111, v92, v93
	v_cvt_pk_bf16_f32 v112, v86, v87
	v_cvt_pk_bf16_f32 v113, v88, v89
	v_cvt_pk_bf16_f32 v114, v82, v83
	v_cvt_pk_bf16_f32 v115, v84, v85
	v_cvt_pk_bf16_f32 v116, v78, v79
	v_cvt_pk_bf16_f32 v117, v80, v81
	v_cvt_pk_bf16_f32 v118, v74, v75
	v_cvt_pk_bf16_f32 v119, v76, v77
	v_cvt_pk_bf16_f32 v120, v70, v71
	v_cvt_pk_bf16_f32 v121, v72, v73
	v_cvt_pk_bf16_f32 v122, v174, v176
	v_cvt_pk_bf16_f32 v123, v68, v69
	v_cvt_pk_bf16_f32 v124, v175, v177
	v_cvt_pk_bf16_f32 v125, v178, v179
	v_cvt_pk_bf16_f32 v126, v180, v182
	v_cvt_pk_bf16_f32 v127, v184, v186
	v_cvt_pk_bf16_f32 v128, v181, v183
	v_cvt_pk_bf16_f32 v129, v185, v187
	v_cvt_pk_bf16_f32 v130, v130, v34
	v_cvt_pk_bf16_f32 v131, v37, v39
	v_cvt_pk_bf16_f32 v132, v30, v33
	v_cvt_pk_bf16_f32 v133, v22, v25
	v_cvt_pk_bf16_f32 v134, v21, v18
	v_cvt_pk_bf16_f32 v135, v27, v29
	v_cvt_pk_bf16_f32 v136, v14, v10
	v_cvt_pk_bf16_f32 v137, v6, v12
	v_cvt_pk_bf16_f32 v138, v36, v35
	v_cvt_pk_bf16_f32 v139, v38, v32
	v_cvt_pk_bf16_f32 v140, v31, v24
	v_cvt_pk_bf16_f32 v141, v23, v20
	v_cvt_pk_bf16_f32 v142, v26, v19
	v_cvt_pk_bf16_f32 v143, v28, v16
	v_cvt_pk_bf16_f32 v144, v15, v11
	v_cvt_pk_bf16_f32 v145, v7, v2
	v_mul_hi_i32 v2, v172, s70
	v_lshrrev_b32_e32 v3, 31, v2
	v_ashrrev_i32_e32 v2, 2, v2
	v_add_u32_e32 v2, v2, v3
	v_mul_lo_u32 v3, v2, 24
	v_sub_u32_e32 v3, v172, v3
	v_lshrrev_b32_e32 v16, 1, v2
	v_bitop3_b32 v3, v16, v3, 7 bitop3:0x6c
	v_mul_lo_u32 v2, v2, s68
	v_lshl_add_u32 v2, v3, 4, v2
	v_add_u32_e32 v3, 0x200, v172
	v_mul_hi_i32 v4, v3, s70
	v_lshrrev_b32_e32 v5, 31, v4
	v_ashrrev_i32_e32 v4, 2, v4
	v_add_u32_e32 v4, v4, v5
	v_mul_lo_u32 v5, v4, 24
	v_sub_u32_e32 v5, v3, v5
	v_lshrrev_b32_e32 v16, 1, v4
	v_bitop3_b32 v5, v16, v5, 7 bitop3:0x6c
	v_mul_lo_u32 v4, v4, s68
	v_lshl_add_u32 v4, v5, 4, v4
	v_add_u32_e32 v5, 0x400, v172
	v_mul_hi_i32 v6, v5, s70
	v_lshrrev_b32_e32 v7, 31, v6
	v_ashrrev_i32_e32 v6, 2, v6
	v_add_u32_e32 v6, v6, v7
	v_mul_lo_u32 v7, v6, 24
	v_sub_u32_e32 v5, v5, v7
	v_lshrrev_b32_e32 v16, 1, v6
	v_bitop3_b32 v5, v16, v5, 7 bitop3:0x6c
	v_mul_lo_u32 v6, v6, s68
	v_ashrrev_i32_e32 v9, 4, v172
	v_lshl_add_u32 v6, v5, 4, v6
	v_bfe_u32 v5, v172, 2, 2
	v_lshrrev_b32_e32 v7, 1, v172
	v_and_b32_e32 v10, 0x1ffff0, v9
	v_lshrrev_b32_e32 v9, 1, v9
	v_ashrrev_i32_e32 v3, 4, v3
	v_and_or_b32 v5, v7, 8, v5
	v_and_b32_e32 v7, 0x60, v172
	v_lshlrev_b32_e32 v8, 3, v172
	v_and_b32_e32 v9, 4, v9
	v_and_b32_e32 v11, 0x1ffff0, v3
	v_lshrrev_b32_e32 v3, 1, v3
	v_and_or_b32 v7, v8, 24, v7
	v_or3_b32 v9, v10, v9, v5
	v_and_b32_e32 v3, 4, v3
	s_barrier
	global_load_lds_dwordx4 v2, s[44:45]
	s_mov_b32 m0, s72
	v_lshlrev_b32_e32 v7, 1, v7
	v_lshlrev_b32_e32 v10, 11, v9
	v_or3_b32 v3, v11, v3, v5
	global_load_lds_dwordx4 v4, s[44:45]
	s_mov_b32 m0, s73
	v_or_b32_e32 v9, v10, v7
	v_lshlrev_b32_e32 v11, 11, v3
	global_load_lds_dwordx4 v6, s[44:45]
	s_mov_b32 m0, s64
	v_or_b32_e32 v3, v11, v7
	global_load_lds_dwordx4 v9, s[46:47]
	s_mov_b32 m0, s74
	v_lshlrev_b32_e32 v13, 1, v172
	global_load_lds_dwordx4 v3, s[46:47]
	v_lshlrev_b32_e32 v9, 4, v172
	v_and_b32_e32 v14, 32, v13
	v_or_b32_e32 v3, 32, v148
	v_and_b32_e32 v16, 0x13, v168
	v_and_b32_e32 v17, 4, v168
	v_lshl_or_b32 v16, v17, 1, v16
	v_and_b32_e32 v17, 8, v168
	v_lshrrev_b32_e32 v17, 1, v17
	v_or_b32_e32 v16, v16, v17
	v_mul_u32_u24_e32 v5, 0x180, v16
	v_lshlrev_b32_e32 v17, 3, v16
	v_and_b32_e32 v7, 0x70, v17
	v_and_b32_e32 v12, 0xc0, v9
	v_and_or_b32 v8, v8, s75, v14
	v_and_b32_e32 v167, 63, v172
	v_bitop3_b32 v169, v3, v5, v7 bitop3:0xde
	v_or_b32_e32 v3, 64, v148
	v_add3_u32 v172, v12, 0, v8
	v_and_b32_e32 v12, 0xc0, v13
	v_and_b32_e32 v13, 48, v9
	v_bitop3_b32 v170, v3, v5, v7 bitop3:0xde
	v_or_b32_e32 v3, 0x60, v148
	v_or3_b32 v8, v11, v12, v13
	v_mov_b32_e32 v9, v149
	v_bitop3_b32 v161, v148, v5, v7 bitop3:0xde
	v_bitop3_b32 v171, v3, v5, v7 bitop3:0xde
	v_mov_b32_e32 v3, v149
	v_mov_b32_e32 v5, v149
	v_mov_b32_e32 v7, v149
	v_mul_i32_i24_e32 v15, -8, v173
	v_lshl_add_u64 v[150:151], s[48:49], 0, v[8:9]
	v_mov_b32_e32 v240, v8
	v_or3_b32 v8, v10, v12, v13
	v_mov_b32_e32 v16, v149
	v_mov_b32_e32 v17, v149
	v_lshl_add_u32 v160, v168, 2, s65
	v_lshl_add_u64 v[152:153], s[48:49], 0, v[8:9]
	v_mov_b32_e32 v241, v8
	v_lshl_add_u64 v[154:155], s[50:51], 0, v[6:7]
	v_mov_b32_e32 v242, v6
	v_lshl_add_u64 v[156:157], s[50:51], 0, v[4:5]
	v_mov_b32_e32 v243, v4
	v_lshl_add_u64 v[158:159], s[50:51], 0, v[2:3]
	v_mov_b32_e32 v244, v2
	s_add_u32 s94, s2, s50
	s_addc_u32 s95, s3, s51
	s_add_u32 s96, s2, s48
	s_addc_u32 s97, s3, s49
	v_add3_u32 v168, s63, v15, v168
	v_mov_b32_e32 v2, v149
	v_mov_b32_e32 v4, v149
	v_mov_b32_e32 v6, v149
	v_mov_b32_e32 v8, v149
	v_mov_b32_e32 v10, v149
	v_mov_b32_e32 v11, v149
	v_mov_b32_e32 v12, v149
	v_mov_b32_e32 v13, v149
	v_mov_b32_e32 v14, v149
	v_mov_b32_e32 v15, v149
	v_mov_b32_e32 v32, v16
	v_mov_b32_e32 v33, v17
	v_mov_b32_e32 v48, v16
	v_mov_b32_e32 v49, v17
	v_mov_b32_e32 v64, v16
	v_mov_b32_e32 v65, v17
	v_cmp_gt_u32_e64 s[0:1], 32, v167
	v_mov_b32_e32 v173, 0
	v_mov_b32_e32 v206, 0
	v_mov_b32_e32 v207, 0
	v_mov_b32_e32 v208, 0
	v_mov_b32_e32 v209, 0
	v_mov_b32_e32 v210, 0
	v_mov_b32_e32 v211, 0
	v_mov_b32_e32 v212, 0
	v_mov_b32_e32 v213, 0
	v_mov_b32_e32 v214, 0
	v_mov_b32_e32 v215, 0
	v_mov_b32_e32 v216, 0
	v_mov_b32_e32 v217, 0
	v_mov_b32_e32 v218, 0
	v_mov_b32_e32 v219, 0
	v_mov_b32_e32 v220, 0
	v_mov_b32_e32 v221, 0
	v_mov_b32_e32 v30, v14
	v_mov_b32_e32 v31, v15
	v_mov_b32_e32 v28, v12
	v_mov_b32_e32 v29, v13
	v_mov_b32_e32 v26, v10
	v_mov_b32_e32 v27, v11
	v_mov_b32_e32 v24, v8
	v_mov_b32_e32 v25, v9
	v_mov_b32_e32 v22, v6
	v_mov_b32_e32 v23, v7
	v_mov_b32_e32 v20, v4
	v_mov_b32_e32 v21, v5
	v_mov_b32_e32 v18, v2
	v_mov_b32_e32 v19, v3
	v_mov_b32_e32 v46, v14
	v_mov_b32_e32 v47, v15
	v_mov_b32_e32 v44, v12
	v_mov_b32_e32 v45, v13
	v_mov_b32_e32 v42, v10
	v_mov_b32_e32 v43, v11
	v_mov_b32_e32 v40, v8
	v_mov_b32_e32 v41, v9
	v_mov_b32_e32 v38, v6
	v_mov_b32_e32 v39, v7
	v_mov_b32_e32 v36, v4
	v_mov_b32_e32 v37, v5
	v_mov_b32_e32 v34, v2
	v_mov_b32_e32 v35, v3
	v_mov_b32_e32 v62, v14
	v_mov_b32_e32 v63, v15
	v_mov_b32_e32 v60, v12
	v_mov_b32_e32 v61, v13
	v_mov_b32_e32 v58, v10
	v_mov_b32_e32 v59, v11
	v_mov_b32_e32 v56, v8
	v_mov_b32_e32 v57, v9
	v_mov_b32_e32 v54, v6
	v_mov_b32_e32 v55, v7
	v_mov_b32_e32 v52, v4
	v_mov_b32_e32 v53, v5
	v_mov_b32_e32 v50, v2
	v_mov_b32_e32 v51, v3
	v_mov_b32_e32 v174, 0

.LBB0_817:
	s_or_b64 exec, exec, s[56:57]
	s_waitcnt lgkmcnt(0)
	s_lshl_b64 s[0:1], s[54:55], 11
	s_add_u32 s0, s61, s0
	s_addc_u32 s1, s62, s1
	s_add_u32 s0, s0, s79
	s_addc_u32 s1, s1, 0
	s_mov_b32 s56, 0x05040100
	v_and_b32_e32 v85, 3, v164
	v_lshl_add_u32 v83, v85, 8, v85
	v_add_u32_e32 v83, 0x0c0c0400, v83
	v_lshrrev_b32_e32 v87, 5, v164
	v_lshl_add_u32 v84, v87, 2, v85
	v_lshlrev_b32_e32 v84, 11, v84
	v_and_b32_e32 v85, 28, v164
	v_add_u32_e32 v84, v84, v85
	v_lshl_add_u32 v87, v87, 4, s65
	ds_read_b128 v[66:69], v87 offset:128
	v_mov_b32_e32 v86, v84
	s_waitcnt lgkmcnt(0)
	v_mul_f32_e32 v66, 0x41800000, v66
	v_mul_f32_e32 v67, 0x41800000, v67
	v_mul_f32_e32 v68, 0x41800000, v68
	v_mul_f32_e32 v69, 0x41800000, v69
	v_mul_f32_e32 v70, v50, v66
	v_mul_f32_e32 v71, v51, v67
	v_mul_f32_e32 v72, v52, v68
	v_mul_f32_e32 v73, v53, v69
	v_med3_f32 v70, v70, s77, v166
	v_med3_f32 v71, v71, s77, v166
	v_med3_f32 v72, v72, s77, v166
	v_med3_f32 v73, v73, s77, v166
	v_cvt_pk_fp8_f32 v74, v70, v71
	v_cvt_pk_fp8_f32 v74, v72, v73 op_sel:[0,0,1]
	s_nop 1
	v_mov_b32_dpp v75, v74 quad_perm:[0,0,0,0] row_mask:0xf bank_mask:0xf
	v_mov_b32_dpp v76, v74 quad_perm:[1,1,1,1] row_mask:0xf bank_mask:0xf
	v_mov_b32_dpp v77, v74 quad_perm:[2,2,2,2] row_mask:0xf bank_mask:0xf
	v_mov_b32_dpp v78, v74 quad_perm:[3,3,3,3] row_mask:0xf bank_mask:0xf
	v_perm_b32 v80, v76, v75, v83
	v_perm_b32 v81, v78, v77, v83
	v_perm_b32 v82, v81, v80, s56
	global_store_dword v86, v82, s[0:1]
	v_mul_f32_e32 v70, v34, v66
	v_mul_f32_e32 v71, v35, v67
	v_mul_f32_e32 v72, v36, v68
	v_mul_f32_e32 v73, v37, v69
	v_med3_f32 v70, v70, s77, v166
	v_med3_f32 v71, v71, s77, v166
	v_med3_f32 v72, v72, s77, v166
	v_med3_f32 v73, v73, s77, v166
	v_cvt_pk_fp8_f32 v74, v70, v71
	v_cvt_pk_fp8_f32 v74, v72, v73 op_sel:[0,0,1]
	s_nop 1
	v_mov_b32_dpp v75, v74 quad_perm:[0,0,0,0] row_mask:0xf bank_mask:0xf
	v_mov_b32_dpp v76, v74 quad_perm:[1,1,1,1] row_mask:0xf bank_mask:0xf
	v_mov_b32_dpp v77, v74 quad_perm:[2,2,2,2] row_mask:0xf bank_mask:0xf
	v_mov_b32_dpp v78, v74 quad_perm:[3,3,3,3] row_mask:0xf bank_mask:0xf
	v_perm_b32 v80, v76, v75, v83
	v_perm_b32 v81, v78, v77, v83
	v_perm_b32 v82, v81, v80, s56
	global_store_dword v86, v82, s[0:1] offset:32
	v_mul_f32_e32 v70, v18, v66
	v_mul_f32_e32 v71, v19, v67
	v_mul_f32_e32 v72, v20, v68
	v_mul_f32_e32 v73, v21, v69
	v_med3_f32 v70, v70, s77, v166
	v_med3_f32 v71, v71, s77, v166
	v_med3_f32 v72, v72, s77, v166
	v_med3_f32 v73, v73, s77, v166
	v_cvt_pk_fp8_f32 v74, v70, v71
	v_cvt_pk_fp8_f32 v74, v72, v73 op_sel:[0,0,1]
	s_nop 1
	v_mov_b32_dpp v75, v74 quad_perm:[0,0,0,0] row_mask:0xf bank_mask:0xf
	v_mov_b32_dpp v76, v74 quad_perm:[1,1,1,1] row_mask:0xf bank_mask:0xf
	v_mov_b32_dpp v77, v74 quad_perm:[2,2,2,2] row_mask:0xf bank_mask:0xf
	v_mov_b32_dpp v78, v74 quad_perm:[3,3,3,3] row_mask:0xf bank_mask:0xf
	v_perm_b32 v80, v76, v75, v83
	v_perm_b32 v81, v78, v77, v83
	v_perm_b32 v82, v81, v80, s56
	global_store_dword v86, v82, s[0:1] offset:64
	v_mul_f32_e32 v70, v2, v66
	v_mul_f32_e32 v71, v3, v67
	v_mul_f32_e32 v72, v4, v68
	v_mul_f32_e32 v73, v5, v69
	v_med3_f32 v70, v70, s77, v166
	v_med3_f32 v71, v71, s77, v166
	v_med3_f32 v72, v72, s77, v166
	v_med3_f32 v73, v73, s77, v166
	v_cvt_pk_fp8_f32 v74, v70, v71
	v_cvt_pk_fp8_f32 v74, v72, v73 op_sel:[0,0,1]
	s_nop 1
	v_mov_b32_dpp v75, v74 quad_perm:[0,0,0,0] row_mask:0xf bank_mask:0xf
	v_mov_b32_dpp v76, v74 quad_perm:[1,1,1,1] row_mask:0xf bank_mask:0xf
	v_mov_b32_dpp v77, v74 quad_perm:[2,2,2,2] row_mask:0xf bank_mask:0xf
	v_mov_b32_dpp v78, v74 quad_perm:[3,3,3,3] row_mask:0xf bank_mask:0xf
	v_perm_b32 v80, v76, v75, v83
	v_perm_b32 v81, v78, v77, v83
	v_perm_b32 v82, v81, v80, s56
	global_store_dword v86, v82, s[0:1] offset:96
	ds_read_b128 v[66:69], v87 offset:160
	v_add_u32_e32 v86, 0x4000, v84
	s_waitcnt lgkmcnt(0)
	v_mul_f32_e32 v66, 0x41800000, v66
	v_mul_f32_e32 v67, 0x41800000, v67
	v_mul_f32_e32 v68, 0x41800000, v68
	v_mul_f32_e32 v69, 0x41800000, v69
	v_mul_f32_e32 v70, v54, v66
	v_mul_f32_e32 v71, v55, v67
	v_mul_f32_e32 v72, v56, v68
	v_mul_f32_e32 v73, v57, v69
	v_med3_f32 v70, v70, s77, v166
	v_med3_f32 v71, v71, s77, v166
	v_med3_f32 v72, v72, s77, v166
	v_med3_f32 v73, v73, s77, v166
	v_cvt_pk_fp8_f32 v74, v70, v71
	v_cvt_pk_fp8_f32 v74, v72, v73 op_sel:[0,0,1]
	s_nop 1
	v_mov_b32_dpp v75, v74 quad_perm:[0,0,0,0] row_mask:0xf bank_mask:0xf
	v_mov_b32_dpp v76, v74 quad_perm:[1,1,1,1] row_mask:0xf bank_mask:0xf
	v_mov_b32_dpp v77, v74 quad_perm:[2,2,2,2] row_mask:0xf bank_mask:0xf
	v_mov_b32_dpp v78, v74 quad_perm:[3,3,3,3] row_mask:0xf bank_mask:0xf
	v_perm_b32 v80, v76, v75, v83
	v_perm_b32 v81, v78, v77, v83
	v_perm_b32 v82, v81, v80, s56
	global_store_dword v86, v82, s[0:1]
	v_mul_f32_e32 v70, v38, v66
	v_mul_f32_e32 v71, v39, v67
	v_mul_f32_e32 v72, v40, v68
	v_mul_f32_e32 v73, v41, v69
	v_med3_f32 v70, v70, s77, v166
	v_med3_f32 v71, v71, s77, v166
	v_med3_f32 v72, v72, s77, v166
	v_med3_f32 v73, v73, s77, v166
	v_cvt_pk_fp8_f32 v74, v70, v71
	v_cvt_pk_fp8_f32 v74, v72, v73 op_sel:[0,0,1]
	s_nop 1
	v_mov_b32_dpp v75, v74 quad_perm:[0,0,0,0] row_mask:0xf bank_mask:0xf
	v_mov_b32_dpp v76, v74 quad_perm:[1,1,1,1] row_mask:0xf bank_mask:0xf
	v_mov_b32_dpp v77, v74 quad_perm:[2,2,2,2] row_mask:0xf bank_mask:0xf
	v_mov_b32_dpp v78, v74 quad_perm:[3,3,3,3] row_mask:0xf bank_mask:0xf
	v_perm_b32 v80, v76, v75, v83
	v_perm_b32 v81, v78, v77, v83
	v_perm_b32 v82, v81, v80, s56
	global_store_dword v86, v82, s[0:1] offset:32
	v_mul_f32_e32 v70, v22, v66
	v_mul_f32_e32 v71, v23, v67
	v_mul_f32_e32 v72, v24, v68
	v_mul_f32_e32 v73, v25, v69
	v_med3_f32 v70, v70, s77, v166
	v_med3_f32 v71, v71, s77, v166
	v_med3_f32 v72, v72, s77, v166
	v_med3_f32 v73, v73, s77, v166
	v_cvt_pk_fp8_f32 v74, v70, v71
	v_cvt_pk_fp8_f32 v74, v72, v73 op_sel:[0,0,1]
	s_nop 1
	v_mov_b32_dpp v75, v74 quad_perm:[0,0,0,0] row_mask:0xf bank_mask:0xf
	v_mov_b32_dpp v76, v74 quad_perm:[1,1,1,1] row_mask:0xf bank_mask:0xf
	v_mov_b32_dpp v77, v74 quad_perm:[2,2,2,2] row_mask:0xf bank_mask:0xf
	v_mov_b32_dpp v78, v74 quad_perm:[3,3,3,3] row_mask:0xf bank_mask:0xf
	v_perm_b32 v80, v76, v75, v83
	v_perm_b32 v81, v78, v77, v83
	v_perm_b32 v82, v81, v80, s56
	global_store_dword v86, v82, s[0:1] offset:64
	v_mul_f32_e32 v70, v6, v66
	v_mul_f32_e32 v71, v7, v67
	v_mul_f32_e32 v72, v8, v68
	v_mul_f32_e32 v73, v9, v69
	v_med3_f32 v70, v70, s77, v166
	v_med3_f32 v71, v71, s77, v166
	v_med3_f32 v72, v72, s77, v166
	v_med3_f32 v73, v73, s77, v166
	v_cvt_pk_fp8_f32 v74, v70, v71
	v_cvt_pk_fp8_f32 v74, v72, v73 op_sel:[0,0,1]
	s_nop 1
	v_mov_b32_dpp v75, v74 quad_perm:[0,0,0,0] row_mask:0xf bank_mask:0xf
	v_mov_b32_dpp v76, v74 quad_perm:[1,1,1,1] row_mask:0xf bank_mask:0xf
	v_mov_b32_dpp v77, v74 quad_perm:[2,2,2,2] row_mask:0xf bank_mask:0xf
	v_mov_b32_dpp v78, v74 quad_perm:[3,3,3,3] row_mask:0xf bank_mask:0xf
	v_perm_b32 v80, v76, v75, v83
	v_perm_b32 v81, v78, v77, v83
	v_perm_b32 v82, v81, v80, s56
	global_store_dword v86, v82, s[0:1] offset:96
	ds_read_b128 v[66:69], v87 offset:192
	v_add_u32_e32 v86, 0x8000, v84
	s_waitcnt lgkmcnt(0)
	v_mul_f32_e32 v66, 0x41800000, v66
	v_mul_f32_e32 v67, 0x41800000, v67
	v_mul_f32_e32 v68, 0x41800000, v68
	v_mul_f32_e32 v69, 0x41800000, v69
	v_mul_f32_e32 v70, v58, v66
	v_mul_f32_e32 v71, v59, v67
	v_mul_f32_e32 v72, v60, v68
	v_mul_f32_e32 v73, v61, v69
	v_med3_f32 v70, v70, s77, v166
	v_med3_f32 v71, v71, s77, v166
	v_med3_f32 v72, v72, s77, v166
	v_med3_f32 v73, v73, s77, v166
	v_cvt_pk_fp8_f32 v74, v70, v71
	v_cvt_pk_fp8_f32 v74, v72, v73 op_sel:[0,0,1]
	s_nop 1
	v_mov_b32_dpp v75, v74 quad_perm:[0,0,0,0] row_mask:0xf bank_mask:0xf
	v_mov_b32_dpp v76, v74 quad_perm:[1,1,1,1] row_mask:0xf bank_mask:0xf
	v_mov_b32_dpp v77, v74 quad_perm:[2,2,2,2] row_mask:0xf bank_mask:0xf
	v_mov_b32_dpp v78, v74 quad_perm:[3,3,3,3] row_mask:0xf bank_mask:0xf
	v_perm_b32 v80, v76, v75, v83
	v_perm_b32 v81, v78, v77, v83
	v_perm_b32 v82, v81, v80, s56
	global_store_dword v86, v82, s[0:1]
	v_mul_f32_e32 v70, v42, v66
	v_mul_f32_e32 v71, v43, v67
	v_mul_f32_e32 v72, v44, v68
	v_mul_f32_e32 v73, v45, v69
	v_med3_f32 v70, v70, s77, v166
	v_med3_f32 v71, v71, s77, v166
	v_med3_f32 v72, v72, s77, v166
	v_med3_f32 v73, v73, s77, v166
	v_cvt_pk_fp8_f32 v74, v70, v71
	v_cvt_pk_fp8_f32 v74, v72, v73 op_sel:[0,0,1]
	s_nop 1
	v_mov_b32_dpp v75, v74 quad_perm:[0,0,0,0] row_mask:0xf bank_mask:0xf
	v_mov_b32_dpp v76, v74 quad_perm:[1,1,1,1] row_mask:0xf bank_mask:0xf
	v_mov_b32_dpp v77, v74 quad_perm:[2,2,2,2] row_mask:0xf bank_mask:0xf
	v_mov_b32_dpp v78, v74 quad_perm:[3,3,3,3] row_mask:0xf bank_mask:0xf
	v_perm_b32 v80, v76, v75, v83
	v_perm_b32 v81, v78, v77, v83
	v_perm_b32 v82, v81, v80, s56
	global_store_dword v86, v82, s[0:1] offset:32
	v_mul_f32_e32 v70, v26, v66
	v_mul_f32_e32 v71, v27, v67
	v_mul_f32_e32 v72, v28, v68
	v_mul_f32_e32 v73, v29, v69
	v_med3_f32 v70, v70, s77, v166
	v_med3_f32 v71, v71, s77, v166
	v_med3_f32 v72, v72, s77, v166
	v_med3_f32 v73, v73, s77, v166
	v_cvt_pk_fp8_f32 v74, v70, v71
	v_cvt_pk_fp8_f32 v74, v72, v73 op_sel:[0,0,1]
	s_nop 1
	v_mov_b32_dpp v75, v74 quad_perm:[0,0,0,0] row_mask:0xf bank_mask:0xf
	v_mov_b32_dpp v76, v74 quad_perm:[1,1,1,1] row_mask:0xf bank_mask:0xf
	v_mov_b32_dpp v77, v74 quad_perm:[2,2,2,2] row_mask:0xf bank_mask:0xf
	v_mov_b32_dpp v78, v74 quad_perm:[3,3,3,3] row_mask:0xf bank_mask:0xf
	v_perm_b32 v80, v76, v75, v83
	v_perm_b32 v81, v78, v77, v83
	v_perm_b32 v82, v81, v80, s56
	global_store_dword v86, v82, s[0:1] offset:64
	v_mul_f32_e32 v70, v10, v66
	v_mul_f32_e32 v71, v11, v67
	v_mul_f32_e32 v72, v12, v68
	v_mul_f32_e32 v73, v13, v69
	v_med3_f32 v70, v70, s77, v166
	v_med3_f32 v71, v71, s77, v166
	v_med3_f32 v72, v72, s77, v166
	v_med3_f32 v73, v73, s77, v166
	v_cvt_pk_fp8_f32 v74, v70, v71
	v_cvt_pk_fp8_f32 v74, v72, v73 op_sel:[0,0,1]
	s_nop 1
	v_mov_b32_dpp v75, v74 quad_perm:[0,0,0,0] row_mask:0xf bank_mask:0xf
	v_mov_b32_dpp v76, v74 quad_perm:[1,1,1,1] row_mask:0xf bank_mask:0xf
	v_mov_b32_dpp v77, v74 quad_perm:[2,2,2,2] row_mask:0xf bank_mask:0xf
	v_mov_b32_dpp v78, v74 quad_perm:[3,3,3,3] row_mask:0xf bank_mask:0xf
	v_perm_b32 v80, v76, v75, v83
	v_perm_b32 v81, v78, v77, v83
	v_perm_b32 v82, v81, v80, s56
	global_store_dword v86, v82, s[0:1] offset:96
	ds_read_b128 v[66:69], v87 offset:224
	v_add_u32_e32 v86, 0xc000, v84
	s_waitcnt lgkmcnt(0)
	v_mul_f32_e32 v66, 0x41800000, v66
	v_mul_f32_e32 v67, 0x41800000, v67
	v_mul_f32_e32 v68, 0x41800000, v68
	v_mul_f32_e32 v69, 0x41800000, v69
	v_mul_f32_e32 v70, v62, v66
	v_mul_f32_e32 v71, v63, v67
	v_mul_f32_e32 v72, v64, v68
	v_mul_f32_e32 v73, v65, v69
	v_med3_f32 v70, v70, s77, v166
	v_med3_f32 v71, v71, s77, v166
	v_med3_f32 v72, v72, s77, v166
	v_med3_f32 v73, v73, s77, v166
	v_cvt_pk_fp8_f32 v74, v70, v71
	v_cvt_pk_fp8_f32 v74, v72, v73 op_sel:[0,0,1]
	s_nop 1
	v_mov_b32_dpp v75, v74 quad_perm:[0,0,0,0] row_mask:0xf bank_mask:0xf
	v_mov_b32_dpp v76, v74 quad_perm:[1,1,1,1] row_mask:0xf bank_mask:0xf
	v_mov_b32_dpp v77, v74 quad_perm:[2,2,2,2] row_mask:0xf bank_mask:0xf
	v_mov_b32_dpp v78, v74 quad_perm:[3,3,3,3] row_mask:0xf bank_mask:0xf
	v_perm_b32 v80, v76, v75, v83
	v_perm_b32 v81, v78, v77, v83
	v_perm_b32 v82, v81, v80, s56
	global_store_dword v86, v82, s[0:1]
	v_mul_f32_e32 v70, v46, v66
	v_mul_f32_e32 v71, v47, v67
	v_mul_f32_e32 v72, v48, v68
	v_mul_f32_e32 v73, v49, v69
	v_med3_f32 v70, v70, s77, v166
	v_med3_f32 v71, v71, s77, v166
	v_med3_f32 v72, v72, s77, v166
	v_med3_f32 v73, v73, s77, v166
	v_cvt_pk_fp8_f32 v74, v70, v71
	v_cvt_pk_fp8_f32 v74, v72, v73 op_sel:[0,0,1]
	s_nop 1
	v_mov_b32_dpp v75, v74 quad_perm:[0,0,0,0] row_mask:0xf bank_mask:0xf
	v_mov_b32_dpp v76, v74 quad_perm:[1,1,1,1] row_mask:0xf bank_mask:0xf
	v_mov_b32_dpp v77, v74 quad_perm:[2,2,2,2] row_mask:0xf bank_mask:0xf
	v_mov_b32_dpp v78, v74 quad_perm:[3,3,3,3] row_mask:0xf bank_mask:0xf
	v_perm_b32 v80, v76, v75, v83
	v_perm_b32 v81, v78, v77, v83
	v_perm_b32 v82, v81, v80, s56
	global_store_dword v86, v82, s[0:1] offset:32
	v_mul_f32_e32 v70, v30, v66
	v_mul_f32_e32 v71, v31, v67
	v_mul_f32_e32 v72, v32, v68
	v_mul_f32_e32 v73, v33, v69
	v_med3_f32 v70, v70, s77, v166
	v_med3_f32 v71, v71, s77, v166
	v_med3_f32 v72, v72, s77, v166
	v_med3_f32 v73, v73, s77, v166
	v_cvt_pk_fp8_f32 v74, v70, v71
	v_cvt_pk_fp8_f32 v74, v72, v73 op_sel:[0,0,1]
	s_nop 1
	v_mov_b32_dpp v75, v74 quad_perm:[0,0,0,0] row_mask:0xf bank_mask:0xf
	v_mov_b32_dpp v76, v74 quad_perm:[1,1,1,1] row_mask:0xf bank_mask:0xf
	v_mov_b32_dpp v77, v74 quad_perm:[2,2,2,2] row_mask:0xf bank_mask:0xf
	v_mov_b32_dpp v78, v74 quad_perm:[3,3,3,3] row_mask:0xf bank_mask:0xf
	v_perm_b32 v80, v76, v75, v83
	v_perm_b32 v81, v78, v77, v83
	v_perm_b32 v82, v81, v80, s56
	global_store_dword v86, v82, s[0:1] offset:64
	v_mul_f32_e32 v70, v14, v66
	v_mul_f32_e32 v71, v15, v67
	v_mul_f32_e32 v72, v16, v68
	v_mul_f32_e32 v73, v17, v69
	v_med3_f32 v70, v70, s77, v166
	v_med3_f32 v71, v71, s77, v166
	v_med3_f32 v72, v72, s77, v166
	v_med3_f32 v73, v73, s77, v166
	v_cvt_pk_fp8_f32 v74, v70, v71
	v_cvt_pk_fp8_f32 v74, v72, v73 op_sel:[0,0,1]
	s_nop 1
	v_mov_b32_dpp v75, v74 quad_perm:[0,0,0,0] row_mask:0xf bank_mask:0xf
	v_mov_b32_dpp v76, v74 quad_perm:[1,1,1,1] row_mask:0xf bank_mask:0xf
	v_mov_b32_dpp v77, v74 quad_perm:[2,2,2,2] row_mask:0xf bank_mask:0xf
	v_mov_b32_dpp v78, v74 quad_perm:[3,3,3,3] row_mask:0xf bank_mask:0xf
	v_perm_b32 v80, v76, v75, v83
	v_perm_b32 v81, v78, v77, v83
	v_perm_b32 v82, v81, v80, s56
	global_store_dword v86, v82, s[0:1] offset:96


	s_lshl_b32 s55, s80, 8
	s_and_b32 s0, s81, 15
	s_add_i32 s55, s55, s63
	s_lshl_b32 s54, s0, 8
	v_mov_b32_e32 v168, v1
	s_ashr_i32 s0, s55, 31
	s_add_u32 s52, s52, s55
	v_and_b32_e32 v167, 31, v168
	v_or_b32_e32 v30, s52, v167
	v_mov_b64_e32 v[2:3], s[6:7]
	s_addc_u32 s53, s53, s0
	v_mad_u64_u32 v[2:3], s[0:1], v30, s68, v[2:3]
	v_bfe_u32 v169, v168, 5, 1
	v_mad_i32_i24 v3, s53, v162, v3
	s_lshl_b32 s12, s82, 1
	v_lshl_add_u64 v[2:3], v[2:3], 0, s[12:13]
	v_lshlrev_b32_e32 v148, 4, v169
	v_lshl_add_u64 v[44:45], v[2:3], 0, v[148:149]
	global_load_dwordx4 v[32:35], v[44:45], off
	global_load_dwordx4 v[36:39], v[44:45], off offset:32
	global_load_dwordx4 v[26:29], v[44:45], off offset:64
	global_load_dwordx4 v[22:25], v[44:45], off offset:96
	global_load_dwordx4 v[18:21], v[44:45], off offset:128
	global_load_dwordx4 v[14:17], v[44:45], off offset:160
	global_load_dwordx4 v[10:13], v[44:45], off offset:192
	v_and_b32_e32 v118, 32, v168
	global_load_dwordx4 v[6:9], v118, s[4:5] offset:576
	s_waitcnt lgkmcnt(0)
	global_load_dwordx4 v[2:5], v118, s[4:5] offset:592
	global_load_dwordx4 v[102:105], v118, s[4:5] offset:704
	global_load_dwordx4 v[110:113], v118, s[4:5] offset:720
	global_load_dwordx4 v[40:43], v[44:45], off offset:224
	global_load_dwordx4 v[82:85], v[44:45], off offset:256
	global_load_dwordx4 v[138:141], v[44:45], off offset:288
	global_load_dwordx4 v[70:73], v[44:45], off offset:320
	global_load_dwordx4 v[142:145], v[44:45], off offset:352
	v_mov_b32_e32 v31, s53
	s_mov_b32 m0, s71
	s_mov_b32 s12, 1
	s_waitcnt vmcnt(0)
	v_and_b32_e32 v191, 0xffff0000, v32
	v_lshlrev_b32_e32 v190, 16, v32
	v_lshlrev_b32_e32 v206, 16, v26
	v_and_b32_e32 v207, 0xffff0000, v26
	v_lshlrev_b32_e32 v208, 16, v27
	v_and_b32_e32 v209, 0xffff0000, v27
	v_lshlrev_b32_e32 v210, 16, v28
	v_and_b32_e32 v211, 0xffff0000, v28
	v_lshlrev_b32_e32 v212, 16, v29
	v_and_b32_e32 v213, 0xffff0000, v29
	v_lshlrev_b32_e32 v222, 16, v18
	v_and_b32_e32 v223, 0xffff0000, v18
	v_lshlrev_b32_e32 v224, 16, v19
	v_and_b32_e32 v225, 0xffff0000, v19
	v_lshlrev_b32_e32 v226, 16, v20
	v_and_b32_e32 v227, 0xffff0000, v20
	v_lshlrev_b32_e32 v228, 16, v21
	v_and_b32_e32 v229, 0xffff0000, v21
	global_load_dwordx4 v[26:29], v118, s[4:5] offset:640
	global_load_dwordx4 v[156:159], v118, s[4:5] offset:656
	global_load_dwordx4 v[18:21], v118, s[4:5] offset:528
	v_mul_f32_e32 v188, v191, v191
	v_lshlrev_b32_e32 v192, 16, v33
	v_fmac_f32_e32 v188, v190, v190
	v_and_b32_e32 v193, 0xffff0000, v33
	v_fmac_f32_e32 v188, v192, v192
	v_lshlrev_b32_e32 v194, 16, v34
	v_fmac_f32_e32 v188, v193, v193
	v_and_b32_e32 v195, 0xffff0000, v34
	v_fmac_f32_e32 v188, v194, v194
	v_lshlrev_b32_e32 v196, 16, v35
	v_fmac_f32_e32 v188, v195, v195
	v_and_b32_e32 v197, 0xffff0000, v35
	v_fmac_f32_e32 v188, v196, v196
	v_lshlrev_b32_e32 v198, 16, v36
	v_fmac_f32_e32 v188, v197, v197
	v_and_b32_e32 v199, 0xffff0000, v36
	v_fmac_f32_e32 v188, v198, v198
	v_lshlrev_b32_e32 v200, 16, v37
	v_lshlrev_b32_e32 v214, 16, v22
	v_and_b32_e32 v215, 0xffff0000, v22
	v_lshlrev_b32_e32 v216, 16, v23
	v_and_b32_e32 v217, 0xffff0000, v23
	v_lshlrev_b32_e32 v218, 16, v24
	v_and_b32_e32 v219, 0xffff0000, v24
	v_lshlrev_b32_e32 v220, 16, v25
	v_and_b32_e32 v221, 0xffff0000, v25
	v_fmac_f32_e32 v188, v199, v199
	global_load_dwordx4 v[22:25], v118, s[4:5] offset:512
	v_and_b32_e32 v201, 0xffff0000, v37
	v_fmac_f32_e32 v188, v200, v200
	v_lshlrev_b32_e32 v202, 16, v38
	v_fmac_f32_e32 v188, v201, v201
	v_and_b32_e32 v203, 0xffff0000, v38
	v_fmac_f32_e32 v188, v202, v202
	v_lshlrev_b32_e32 v204, 16, v39
	v_fmac_f32_e32 v188, v203, v203
	v_and_b32_e32 v205, 0xffff0000, v39
	v_fmac_f32_e32 v188, v204, v204
	v_fmac_f32_e32 v188, v205, v205
	v_fmac_f32_e32 v188, v206, v206
	v_fmac_f32_e32 v188, v207, v207
	v_fmac_f32_e32 v188, v208, v208
	v_fmac_f32_e32 v188, v209, v209
	v_fmac_f32_e32 v188, v210, v210
	v_fmac_f32_e32 v188, v211, v211
	v_fmac_f32_e32 v188, v212, v212
	v_fmac_f32_e32 v188, v213, v213
	v_fmac_f32_e32 v188, v214, v214
	v_fmac_f32_e32 v188, v215, v215
	v_fmac_f32_e32 v188, v216, v216
	v_fmac_f32_e32 v188, v217, v217
	v_fmac_f32_e32 v188, v218, v218
	v_fmac_f32_e32 v188, v219, v219
	v_fmac_f32_e32 v188, v220, v220
	v_fmac_f32_e32 v188, v221, v221
	v_fmac_f32_e32 v188, v222, v222
	v_fmac_f32_e32 v188, v223, v223
	v_fmac_f32_e32 v188, v224, v224
	v_fmac_f32_e32 v188, v225, v225
	v_fmac_f32_e32 v188, v226, v226
	v_fmac_f32_e32 v188, v227, v227
	v_fmac_f32_e32 v188, v228, v228
	v_lshlrev_b32_e32 v230, 16, v14
	v_fmac_f32_e32 v188, v229, v229
	v_and_b32_e32 v231, 0xffff0000, v14
	v_fmac_f32_e32 v188, v230, v230
	v_lshlrev_b32_e32 v232, 16, v15
	v_fmac_f32_e32 v188, v231, v231
	v_and_b32_e32 v233, 0xffff0000, v15
	v_fmac_f32_e32 v188, v232, v232
	v_lshlrev_b32_e32 v234, 16, v16
	v_fmac_f32_e32 v188, v233, v233
	v_and_b32_e32 v235, 0xffff0000, v16
	v_fmac_f32_e32 v188, v234, v234
	v_lshlrev_b32_e32 v246, 16, v40
	v_and_b32_e32 v247, 0xffff0000, v40
	v_lshlrev_b32_e32 v248, 16, v41
	v_and_b32_e32 v249, 0xffff0000, v41
	v_lshlrev_b32_e32 v250, 16, v42
	v_and_b32_e32 v251, 0xffff0000, v42
	v_lshlrev_b32_e32 v252, 16, v43
	v_and_b32_e32 v253, 0xffff0000, v43
	global_load_dwordx4 v[106:109], v118, s[4:5] offset:16
	global_load_dwordx4 v[114:117], v118, s[4:5]
	global_load_dwordx4 v[94:97], v118, s[4:5] offset:80
	global_load_dwordx4 v[98:101], v118, s[4:5] offset:64
	global_load_dwordx4 v[86:89], v118, s[4:5] offset:144
	global_load_dwordx4 v[90:93], v118, s[4:5] offset:128
	global_load_dwordx4 v[74:77], v118, s[4:5] offset:208
	global_load_dwordx4 v[78:81], v118, s[4:5] offset:192
	global_load_dwordx4 v[62:65], v118, s[4:5] offset:272
	global_load_dwordx4 v[66:69], v118, s[4:5] offset:256
	global_load_dwordx4 v[54:57], v118, s[4:5] offset:336
	global_load_dwordx4 v[58:61], v118, s[4:5] offset:320
	global_load_dwordx4 v[46:49], v118, s[4:5] offset:400
	global_load_dwordx4 v[50:53], v118, s[4:5] offset:384
	global_load_dwordx4 v[38:41], v118, s[4:5] offset:464
	global_load_dwordx4 v[42:45], v118, s[4:5] offset:448
	v_lshlrev_b32_e32 v236, 16, v17
	v_fmac_f32_e32 v188, v235, v235
	v_and_b32_e32 v237, 0xffff0000, v17
	v_fmac_f32_e32 v188, v236, v236
	v_lshlrev_b32_e32 v238, 16, v10
	v_fmac_f32_e32 v188, v237, v237
	v_and_b32_e32 v239, 0xffff0000, v10
	v_fmac_f32_e32 v188, v238, v238
	v_lshlrev_b32_e32 v240, 16, v11
	v_fmac_f32_e32 v188, v239, v239
	v_and_b32_e32 v241, 0xffff0000, v11
	v_fmac_f32_e32 v188, v240, v240
	v_lshlrev_b32_e32 v242, 16, v12
	v_fmac_f32_e32 v188, v241, v241
	v_and_b32_e32 v243, 0xffff0000, v12
	v_fmac_f32_e32 v188, v242, v242
	v_lshlrev_b32_e32 v244, 16, v13
	v_fmac_f32_e32 v188, v243, v243
	v_and_b32_e32 v245, 0xffff0000, v13
	v_fmac_f32_e32 v188, v244, v244
	v_fmac_f32_e32 v188, v245, v245
	v_fmac_f32_e32 v188, v246, v246
	v_fmac_f32_e32 v188, v247, v247
	v_fmac_f32_e32 v188, v248, v248
	v_fmac_f32_e32 v188, v249, v249
	v_fmac_f32_e32 v188, v250, v250
	v_fmac_f32_e32 v188, v251, v251
	v_fmac_f32_e32 v188, v252, v252
	v_lshlrev_b32_e32 v187, 16, v82
	v_lshlrev_b32_e32 v186, 16, v70
	v_fmac_f32_e32 v188, v253, v253
	v_lshlrev_b32_e32 v124, 16, v144
	v_and_b32_e32 v126, 0xffff0000, v144
	v_lshlrev_b32_e32 v131, 16, v139
	v_and_b32_e32 v133, 0xffff0000, v139
	v_lshlrev_b32_e32 v137, 16, v138
	v_lshlrev_b32_e32 v136, 16, v142
	v_and_b32_e32 v139, 0xffff0000, v138
	v_and_b32_e32 v138, 0xffff0000, v142
	v_lshlrev_b32_e32 v142, 16, v73
	v_and_b32_e32 v144, 0xffff0000, v73
	v_lshlrev_b32_e32 v152, 16, v72
	v_and_b32_e32 v154, 0xffff0000, v72
	v_mul_f32_e32 v72, v186, v186
	v_mul_f32_e32 v73, v187, v187
	s_waitcnt vmcnt(18)
	v_mov_b32_e32 v150, v158
	v_mov_b32_e32 v158, v156
	v_lshlrev_b32_e32 v156, 16, v71
	v_and_b32_e32 v184, 0xffff0000, v71
	v_and_b32_e32 v189, 0xffff0000, v82
	v_add_f32_e32 v71, v73, v188
	v_and_b32_e32 v188, 0xffff0000, v70
	v_mov_b32_e32 v128, v110
	v_mov_b32_e32 v129, v2
	v_mov_b32_e32 v2, v111
	s_waitcnt vmcnt(17)
	v_mov_b32_e32 v151, v20
	v_mov_b32_e32 v20, v159
	v_mov_b32_e32 v159, v18
	v_mov_b32_e32 v18, v157
	v_lshlrev_b32_e32 v157, 16, v83
	v_mul_f32_e32 v110, v188, v188
	v_mul_f32_e32 v111, v189, v189
	v_lshlrev_b32_e32 v119, 16, v141
	v_and_b32_e32 v121, 0xffff0000, v141
	v_lshlrev_b32_e32 v125, 16, v140
	v_and_b32_e32 v127, 0xffff0000, v140
	v_mov_b32_e32 v140, v102
	v_mov_b32_e32 v141, v6
	v_mov_b32_e32 v6, v103
	v_mul_f32_e32 v102, v156, v156
	v_mul_f32_e32 v103, v157, v157
	v_and_b32_e32 v185, 0xffff0000, v83
	v_add_f32_e32 v70, v111, v71
	v_mov_b32_e32 v134, v104
	v_mov_b32_e32 v135, v8
	v_mov_b32_e32 v8, v105
	v_lshlrev_b32_e32 v153, 16, v84
	v_mul_f32_e32 v104, v184, v184
	v_mul_f32_e32 v105, v185, v185
	v_add_f32_e32 v70, v103, v70
	v_mul_f32_e32 v180, v152, v152
	v_mul_f32_e32 v181, v153, v153
	v_and_b32_e32 v155, 0xffff0000, v84
	v_add_f32_e32 v70, v105, v70
	v_lshlrev_b32_e32 v130, 16, v143
	v_and_b32_e32 v132, 0xffff0000, v143
	v_lshlrev_b32_e32 v143, 16, v85
	v_mul_f32_e32 v182, v154, v154
	v_mul_f32_e32 v183, v155, v155
	v_add_f32_e32 v70, v181, v70
	v_lshlrev_b32_e32 v118, 16, v145
	v_and_b32_e32 v120, 0xffff0000, v145
	v_mul_f32_e32 v176, v142, v142
	v_mul_f32_e32 v177, v143, v143
	v_and_b32_e32 v145, 0xffff0000, v85
	v_add_f32_e32 v70, v183, v70
	v_mul_f32_e32 v178, v144, v144
	v_mul_f32_e32 v179, v145, v145
	v_add_f32_e32 v70, v177, v70
	v_mul_f32_e32 v172, v136, v136
	v_mul_f32_e32 v173, v137, v137
	v_add_f32_e32 v70, v179, v70
	v_mul_f32_e32 v174, v138, v138
	v_mul_f32_e32 v175, v139, v139
	v_add_f32_e32 v70, v173, v70
	v_add_f32_e32 v70, v175, v70
	v_fmac_f32_e32 v70, v131, v131
	v_fmac_f32_e32 v70, v133, v133
	v_fmac_f32_e32 v70, v125, v125
	v_fmac_f32_e32 v70, v127, v127
	v_fmac_f32_e32 v70, v119, v119
	v_fmac_f32_e32 v70, v121, v121
	v_add_f32_e32 v103, v72, v70
	v_add_f32_e32 v103, v110, v103
	v_add_f32_e32 v102, v102, v103
	v_add_f32_e32 v173, v104, v102
	v_add_f32_e32 v173, v180, v173
	v_add_f32_e32 v173, v182, v173
	v_add_f32_e32 v173, v176, v173
	v_add_f32_e32 v173, v178, v173
	v_mov_b32_e32 v176, v132
	v_mov_b32_e32 v177, v130
	s_waitcnt vmcnt(16)
	v_mov_b32_e32 v179, v24
	v_add_f32_e32 v24, v172, v173
	v_lshlrev_b64 v[10:11], 8, v[30:31]
	v_mul_f32_e32 v176, v176, v176
	v_mul_f32_e32 v177, v177, v177
	v_add_f32_e32 v24, v174, v24
	v_lshl_add_u64 v[10:11], s[10:11], 0, v[10:11]
	v_lshlrev_b32_e32 v12, 6, v169
	v_mov_b32_e32 v13, v149
	v_mov_b32_e32 v180, v126
	v_mov_b32_e32 v181, v124
	v_add_f32_e32 v24, v177, v24
	v_lshl_add_u64 v[170:171], v[10:11], 0, v[12:13]
	v_mul_f32_e32 v180, v180, v180
	v_mul_f32_e32 v181, v181, v181
	v_add_f32_e32 v24, v176, v24
	global_load_dwordx4 v[10:13], v[170:171], off offset:48
	global_load_dwordx4 v[14:17], v[170:171], off offset:32
	global_load_dwordx4 v[30:33], v[170:171], off offset:16
	global_load_dwordx4 v[34:37], v[170:171], off
	v_mov_b32_e32 v122, v112
	v_mov_b32_e32 v123, v4
	v_mov_b32_e32 v4, v113
	global_load_dwordx4 v[70:73], v[170:171], off offset:176
	global_load_dwordx4 v[82:85], v[170:171], off offset:160
	global_load_dwordx4 v[102:105], v[170:171], off offset:144
	global_load_dwordx4 v[110:113], v[170:171], off offset:128
	v_mov_b32_e32 v170, v120
	v_mov_b32_e32 v171, v118
	v_add_f32_e32 v24, v181, v24
	v_mul_f32_e32 v170, v170, v170
	v_mul_f32_e32 v171, v171, v171
	v_add_f32_e32 v24, v180, v24
	v_add_f32_e32 v24, v171, v24
	v_add_f32_e32 v24, v170, v24
	v_mov_b32_e32 v178, v28
	v_mov_b32_e32 v28, v24
	s_nop 1
	v_permlane32_swap_b32_e32 v24, v28
	v_add_f32_e32 v24, v24, v28
	v_fmamk_f32 v24, v24, 0x3baaaaab, v163
	v_mul_f32_e32 v28, 0x4b800000, v24
	v_cmp_gt_f32_e32 vcc, s69, v24
	s_nop 1
	v_cndmask_b32_e32 v24, v24, v28, vcc
	v_rsq_f32_e32 v170, v24
	v_mov_b32_e32 v24, v29
	v_mov_b32_e32 v29, v22
	v_mov_b32_e32 v28, v26
	v_mul_f32_e32 v22, 0x45800000, v170
	v_cndmask_b32_e32 v22, v170, v22, vcc
	v_mul_f32_e32 v26, 0x3dd53b94, v22
	s_waitcnt vmcnt(22)
	v_mul_f32_e32 v22, v114, v26
	v_mul_f32_e32 v114, v22, v190
	v_mul_f32_e32 v22, v106, v26
	v_mul_f32_e32 v106, v22, v194
	v_mul_f32_e32 v22, v115, v26
	v_mul_f32_e32 v115, v22, v191
	v_mul_f32_e32 v22, v107, v26
	v_mul_f32_e32 v107, v22, v195
	v_mul_f32_e32 v22, v116, v26
	v_mul_f32_e32 v116, v22, v192
	v_mul_f32_e32 v22, v108, v26
	v_mul_f32_e32 v108, v22, v196
	v_mul_f32_e32 v22, v117, v26
	v_mul_f32_e32 v117, v22, v193
	v_mul_f32_e32 v22, v109, v26
	v_mul_f32_e32 v109, v22, v197
	s_waitcnt vmcnt(20)
	v_mul_f32_e32 v22, v98, v26
	v_mul_f32_e32 v170, v22, v198
	v_mul_f32_e32 v22, v94, v26
	v_mul_f32_e32 v94, v22, v202
	v_mul_f32_e32 v22, v99, v26
	v_mul_f32_e32 v171, v22, v199
	v_mul_f32_e32 v22, v95, v26
	v_mul_f32_e32 v95, v22, v203
	v_mul_f32_e32 v22, v100, v26
	v_mul_f32_e32 v172, v22, v200
	v_mul_f32_e32 v22, v96, v26
	v_mul_f32_e32 v96, v22, v204
	v_mul_f32_e32 v22, v101, v26
	v_mul_f32_e32 v173, v22, v201
	v_mul_f32_e32 v22, v97, v26
	v_mul_f32_e32 v97, v22, v205
	s_waitcnt vmcnt(18)
	v_mul_f32_e32 v22, v90, v26
	v_mul_f32_e32 v90, v22, v206
	v_mul_f32_e32 v22, v86, v26
	v_mul_f32_e32 v86, v22, v210
	v_mul_f32_e32 v22, v91, v26
	v_mul_f32_e32 v91, v22, v207
	v_mul_f32_e32 v22, v87, v26
	v_mul_f32_e32 v87, v22, v211
	v_mul_f32_e32 v22, v92, v26
	v_mul_f32_e32 v92, v22, v208
	v_mul_f32_e32 v22, v88, v26
	v_mul_f32_e32 v88, v22, v212
	v_mul_f32_e32 v22, v93, v26
	v_mul_f32_e32 v93, v22, v209
	v_mul_f32_e32 v22, v89, v26
	v_mul_f32_e32 v89, v22, v213
	s_waitcnt vmcnt(16)
	v_mul_f32_e32 v22, v78, v26
	v_mul_f32_e32 v78, v22, v214
	v_mul_f32_e32 v22, v74, v26
	v_mul_f32_e32 v74, v22, v218
	v_mul_f32_e32 v22, v79, v26
	v_mul_f32_e32 v79, v22, v215
	v_mul_f32_e32 v22, v75, v26
	v_mul_f32_e32 v75, v22, v219
	v_mul_f32_e32 v22, v80, v26
	v_mul_f32_e32 v80, v22, v216
	v_mul_f32_e32 v22, v76, v26
	v_mul_f32_e32 v76, v22, v220
	v_mul_f32_e32 v22, v81, v26
	v_mul_f32_e32 v81, v22, v217
	v_mul_f32_e32 v22, v77, v26
	v_mul_f32_e32 v77, v22, v221
	s_waitcnt vmcnt(14)
	v_mul_f32_e32 v22, v66, v26
	v_mul_f32_e32 v66, v22, v222
	v_mul_f32_e32 v22, v26, v62
	v_mul_f32_e32 v62, v22, v226
	v_mul_f32_e32 v22, v67, v26
	v_mul_f32_e32 v67, v22, v223
	v_mul_f32_e32 v22, v26, v63
	v_mul_f32_e32 v63, v22, v227
	v_mul_f32_e32 v22, v68, v26
	v_mul_f32_e32 v68, v22, v224
	v_mul_f32_e32 v22, v26, v64
	v_mul_f32_e32 v64, v22, v228
	v_mul_f32_e32 v22, v69, v26
	v_mul_f32_e32 v69, v22, v225
	v_mul_f32_e32 v22, v26, v65
	v_mul_f32_e32 v65, v22, v229
	s_waitcnt vmcnt(12)
	v_mul_f32_e32 v22, v26, v58
	v_mul_f32_e32 v58, v22, v230
	v_mul_f32_e32 v22, v26, v54
	v_mul_f32_e32 v54, v22, v234
	v_mul_f32_e32 v22, v26, v59
	v_mul_f32_e32 v59, v22, v231
	v_mul_f32_e32 v22, v26, v55
	v_mul_f32_e32 v55, v22, v235
	v_mul_f32_e32 v22, v26, v60
	v_mul_f32_e32 v60, v22, v232
	v_mul_f32_e32 v22, v26, v56
	v_mul_f32_e32 v56, v22, v236
	v_mul_f32_e32 v22, v26, v61
	v_mul_f32_e32 v61, v22, v233
	v_mul_f32_e32 v22, v26, v57
	v_mul_f32_e32 v57, v22, v237
	s_waitcnt vmcnt(10)
	v_mul_f32_e32 v22, v26, v50
	v_mul_f32_e32 v174, v22, v238
	v_mul_f32_e32 v22, v26, v46
	v_mul_f32_e32 v175, v22, v242
	v_mul_f32_e32 v22, v26, v51
	v_mul_f32_e32 v176, v22, v239
	v_mul_f32_e32 v22, v26, v47
	v_mul_f32_e32 v177, v22, v243
	v_mul_f32_e32 v22, v26, v52
	v_mul_f32_e32 v52, v22, v240
	v_mul_f32_e32 v22, v26, v48
	v_mul_f32_e32 v180, v22, v244
	v_mul_f32_e32 v22, v26, v53
	v_mul_f32_e32 v53, v22, v241
	v_mul_f32_e32 v22, v26, v49
	v_mul_f32_e32 v181, v22, v245
	s_waitcnt vmcnt(8)
	v_mul_f32_e32 v22, v26, v42
	v_mul_f32_e32 v182, v22, v246
	v_mul_f32_e32 v22, v26, v38
	v_mul_f32_e32 v183, v22, v250
	v_mul_f32_e32 v22, v26, v43
	v_mul_f32_e32 v190, v22, v247
	v_mul_f32_e32 v22, v26, v39
	v_mul_f32_e32 v191, v22, v251
	v_mul_f32_e32 v22, v26, v44
	v_mul_f32_e32 v192, v22, v248
	v_mul_f32_e32 v22, v26, v40
	v_mul_f32_e32 v193, v22, v252
	v_mul_f32_e32 v22, v26, v45
	v_mul_f32_e32 v194, v22, v249
	v_mul_f32_e32 v22, v26, v41
	v_mul_f32_e32 v28, v26, v28
	v_mul_f32_e32 v29, v26, v29
	v_mul_f32_e32 v195, v22, v253
	v_mul_f32_e32 v28, v28, v186
	v_mul_f32_e32 v29, v29, v187
	v_mov_b32_e32 v22, v27
	v_mul_f32_e32 v38, v26, v158
	v_mul_f32_e32 v39, v26, v159
	v_mul_f32_e32 v22, v26, v22
	v_mul_f32_e32 v23, v26, v23
	v_mul_f32_e32 v18, v26, v18
	v_mul_f32_e32 v19, v26, v19
	v_mul_f32_e32 v40, v26, v178
	v_mul_f32_e32 v41, v26, v179
	v_mul_f32_e32 v42, v26, v150
	v_mul_f32_e32 v43, v26, v151
	v_mul_f32_e32 v24, v26, v24
	v_mul_f32_e32 v25, v26, v25
	v_mul_f32_e32 v20, v26, v20
	v_mul_f32_e32 v21, v26, v21
	v_mul_f32_e32 v44, v26, v140
	v_mul_f32_e32 v45, v26, v141
	v_mul_f32_e32 v46, v26, v128
	v_mul_f32_e32 v47, v26, v129
	v_mul_f32_e32 v6, v26, v6
	v_mul_f32_e32 v7, v26, v7
	v_mul_f32_e32 v2, v26, v2
	v_mul_f32_e32 v3, v26, v3
	v_mul_f32_e32 v48, v26, v134
	v_mul_f32_e32 v49, v26, v135
	v_mul_f32_e32 v50, v26, v122
	v_mul_f32_e32 v51, v26, v123
	v_mul_f32_e32 v8, v26, v8
	v_mul_f32_e32 v9, v26, v9
	v_mul_f32_e32 v4, v26, v4
	v_mul_f32_e32 v5, v26, v5
	s_waitcnt vmcnt(4)
	v_mul_f32_e32 v26, v29, v34
	v_mul_f32_e32 v27, v28, v35
	v_mul_f32_e32 v22, v22, v188
	v_mul_f32_e32 v23, v23, v189
	v_mul_f32_e32 v48, v48, v130
	v_mul_f32_e32 v49, v49, v131
	v_sub_f32_e32 v130, v26, v27
	v_mul_f32_e32 v26, v28, v34
	v_mul_f32_e32 v27, v29, v35
	v_mul_f32_e32 v40, v40, v156
	v_mul_f32_e32 v41, v41, v157
	v_add_f32_e32 v28, v27, v26
	v_mul_f32_e32 v26, v23, v36
	v_mul_f32_e32 v27, v22, v37
	v_mul_f32_e32 v22, v22, v36
	v_mul_f32_e32 v23, v23, v37
	v_sub_f32_e32 v26, v26, v27
	v_add_f32_e32 v27, v23, v22
	v_mul_f32_e32 v22, v41, v30
	v_mul_f32_e32 v23, v40, v31
	v_mul_f32_e32 v24, v24, v184
	v_mul_f32_e32 v25, v25, v185
	v_sub_f32_e32 v29, v22, v23
	v_mul_f32_e32 v22, v40, v30
	v_mul_f32_e32 v23, v41, v31
	v_mul_f32_e32 v38, v38, v152
	v_mul_f32_e32 v39, v39, v153
	v_add_f32_e32 v30, v23, v22
	v_mul_f32_e32 v22, v25, v32
	v_mul_f32_e32 v23, v24, v33
	v_sub_f32_e32 v31, v22, v23
	v_mul_f32_e32 v22, v24, v32
	v_mul_f32_e32 v23, v25, v33
	v_mul_f32_e32 v18, v18, v154
	v_mul_f32_e32 v19, v19, v155
	v_add_f32_e32 v24, v23, v22
	v_mul_f32_e32 v22, v39, v14
	v_mul_f32_e32 v23, v38, v15
	v_mul_f32_e32 v14, v38, v14
	v_mul_f32_e32 v15, v39, v15
	v_sub_f32_e32 v22, v22, v23
	v_add_f32_e32 v23, v15, v14
	v_mul_f32_e32 v14, v19, v16
	v_mul_f32_e32 v15, v18, v17
	v_mul_f32_e32 v42, v42, v142
	v_mul_f32_e32 v43, v43, v143
	v_sub_f32_e32 v25, v14, v15
	v_mul_f32_e32 v14, v18, v16
	v_mul_f32_e32 v15, v19, v17
	v_mul_f32_e32 v20, v20, v144
	v_mul_f32_e32 v21, v21, v145
	v_add_f32_e32 v16, v15, v14
	v_mul_f32_e32 v14, v43, v10
	v_mul_f32_e32 v15, v42, v11
	v_mul_f32_e32 v10, v42, v10
	v_mul_f32_e32 v11, v43, v11
	v_sub_f32_e32 v14, v14, v15
	v_add_f32_e32 v15, v11, v10
	v_mul_f32_e32 v10, v21, v12
	v_mul_f32_e32 v11, v20, v13
	v_mul_f32_e32 v44, v44, v136
	v_mul_f32_e32 v45, v45, v137
	v_sub_f32_e32 v17, v10, v11
	v_mul_f32_e32 v10, v20, v12
	v_mul_f32_e32 v11, v21, v13
	v_mul_f32_e32 v6, v6, v138
	v_mul_f32_e32 v7, v7, v139
	v_add_f32_e32 v12, v11, v10
	s_waitcnt vmcnt(0)
	v_mul_f32_e32 v10, v45, v110
	v_mul_f32_e32 v11, v44, v111
	v_sub_f32_e32 v13, v10, v11
	v_mul_f32_e32 v10, v44, v110
	v_mul_f32_e32 v11, v45, v111
	v_mul_f32_e32 v8, v8, v132
	v_mul_f32_e32 v9, v9, v133
	v_add_f32_e32 v18, v11, v10
	v_mul_f32_e32 v10, v7, v112
	v_mul_f32_e32 v11, v6, v113
	v_mul_f32_e32 v6, v6, v112
	v_mul_f32_e32 v7, v7, v113
	v_sub_f32_e32 v10, v10, v11
	v_add_f32_e32 v11, v7, v6
	v_mul_f32_e32 v6, v49, v102
	v_mul_f32_e32 v7, v48, v103
	v_sub_f32_e32 v19, v6, v7
	v_mul_f32_e32 v6, v48, v102
	v_mul_f32_e32 v7, v49, v103
	v_mul_f32_e32 v46, v46, v124
	v_mul_f32_e32 v47, v47, v125
	v_add_f32_e32 v20, v7, v6
	v_mul_f32_e32 v6, v9, v104
	v_mul_f32_e32 v7, v8, v105
	v_sub_f32_e32 v21, v6, v7
	v_mul_f32_e32 v6, v8, v104
	v_mul_f32_e32 v7, v9, v105
	v_mul_f32_e32 v2, v2, v126
	v_mul_f32_e32 v3, v3, v127
	v_add_f32_e32 v8, v7, v6
	v_mul_f32_e32 v6, v47, v82
	v_mul_f32_e32 v7, v46, v83
	v_sub_f32_e32 v9, v6, v7
	v_mul_f32_e32 v6, v46, v82
	v_mul_f32_e32 v7, v47, v83
	v_mul_f32_e32 v50, v50, v118
	v_mul_f32_e32 v51, v51, v119
	v_add_f32_e32 v32, v7, v6
	v_mul_f32_e32 v6, v3, v84
	v_mul_f32_e32 v7, v2, v85
	v_mul_f32_e32 v2, v2, v84
	v_mul_f32_e32 v3, v3, v85
	v_sub_f32_e32 v6, v6, v7
	v_add_f32_e32 v7, v3, v2
	v_mul_f32_e32 v2, v51, v70
	v_mul_f32_e32 v3, v50, v71
	v_mul_f32_e32 v4, v4, v120
	v_mul_f32_e32 v5, v5, v121
	v_sub_f32_e32 v33, v2, v3
	v_mul_f32_e32 v2, v50, v70
	v_mul_f32_e32 v3, v51, v71
	v_cvt_pk_bf16_f32 v98, v114, v115
	v_cvt_pk_bf16_f32 v99, v116, v117
	v_cvt_pk_bf16_f32 v100, v106, v107
	v_cvt_pk_bf16_f32 v101, v108, v109
	v_cvt_pk_bf16_f32 v102, v170, v171
	s_nop 0
	v_add_f32_e32 v34, v3, v2
	v_mul_f32_e32 v2, v5, v72
	v_mul_f32_e32 v3, v4, v73
	v_sub_f32_e32 v35, v2, v3
	v_mul_f32_e32 v2, v4, v72
	v_mul_f32_e32 v3, v5, v73
	v_cvt_pk_bf16_f32 v103, v172, v173
	v_cvt_pk_bf16_f32 v104, v94, v95
	v_cvt_pk_bf16_f32 v105, v96, v97
	v_cvt_pk_bf16_f32 v106, v90, v91
	v_cvt_pk_bf16_f32 v107, v92, v93
	s_nop 0
	v_add_f32_e32 v2, v3, v2
	v_cvt_pk_bf16_f32 v108, v86, v87
	v_cvt_pk_bf16_f32 v109, v88, v89
	v_cvt_pk_bf16_f32 v110, v78, v79
	v_cvt_pk_bf16_f32 v111, v80, v81
	v_cvt_pk_bf16_f32 v112, v74, v75
	v_cvt_pk_bf16_f32 v113, v76, v77
	v_cvt_pk_bf16_f32 v114, v66, v67
	v_cvt_pk_bf16_f32 v115, v68, v69
	v_cvt_pk_bf16_f32 v116, v62, v63
	v_cvt_pk_bf16_f32 v117, v64, v65
	v_cvt_pk_bf16_f32 v118, v58, v59
	v_cvt_pk_bf16_f32 v119, v60, v61
	v_cvt_pk_bf16_f32 v120, v54, v55
	v_cvt_pk_bf16_f32 v121, v56, v57
	v_cvt_pk_bf16_f32 v122, v174, v176
	v_cvt_pk_bf16_f32 v123, v52, v53
	v_cvt_pk_bf16_f32 v124, v175, v177
	v_cvt_pk_bf16_f32 v125, v180, v181
	v_cvt_pk_bf16_f32 v126, v182, v190
	v_cvt_pk_bf16_f32 v127, v192, v194
	v_cvt_pk_bf16_f32 v128, v183, v191
	v_cvt_pk_bf16_f32 v129, v193, v195
	v_cvt_pk_bf16_f32 v130, v130, v26
	v_cvt_pk_bf16_f32 v131, v29, v31
	v_cvt_pk_bf16_f32 v132, v22, v25
	v_cvt_pk_bf16_f32 v133, v14, v17
	v_cvt_pk_bf16_f32 v134, v13, v10
	v_cvt_pk_bf16_f32 v135, v19, v21
	v_cvt_pk_bf16_f32 v136, v9, v6
	v_cvt_pk_bf16_f32 v137, v33, v35
	v_cvt_pk_bf16_f32 v138, v28, v27
	v_cvt_pk_bf16_f32 v139, v30, v24
	v_cvt_pk_bf16_f32 v140, v23, v16
	v_cvt_pk_bf16_f32 v141, v15, v12
	v_cvt_pk_bf16_f32 v142, v18, v11
	v_cvt_pk_bf16_f32 v143, v20, v8
	v_cvt_pk_bf16_f32 v144, v32, v7
	v_cvt_pk_bf16_f32 v145, v34, v2
	v_mul_hi_i32 v2, v168, s70
	v_lshrrev_b32_e32 v3, 31, v2
	v_ashrrev_i32_e32 v2, 2, v2
	v_add_u32_e32 v2, v2, v3
	v_mul_lo_u32 v3, v2, 24
	v_sub_u32_e32 v3, v168, v3
	v_lshrrev_b32_e32 v16, 1, v2
	v_bitop3_b32 v3, v16, v3, 7 bitop3:0x6c
	v_mul_lo_u32 v2, v2, s68
	v_lshl_add_u32 v2, v3, 4, v2
	v_add_u32_e32 v3, 0x200, v168
	v_mul_hi_i32 v4, v3, s70
	v_lshrrev_b32_e32 v5, 31, v4
	v_ashrrev_i32_e32 v4, 2, v4
	v_add_u32_e32 v4, v4, v5
	v_mul_lo_u32 v5, v4, 24
	v_sub_u32_e32 v5, v3, v5
	v_lshrrev_b32_e32 v16, 1, v4
	v_bitop3_b32 v5, v16, v5, 7 bitop3:0x6c
	v_mul_lo_u32 v4, v4, s68
	v_lshl_add_u32 v4, v5, 4, v4
	v_add_u32_e32 v5, 0x400, v168
	v_mul_hi_i32 v6, v5, s70
	v_lshrrev_b32_e32 v7, 31, v6
	v_ashrrev_i32_e32 v6, 2, v6
	v_add_u32_e32 v6, v6, v7
	v_mul_lo_u32 v7, v6, 24
	v_sub_u32_e32 v5, v5, v7
	v_lshrrev_b32_e32 v16, 1, v6
	v_bitop3_b32 v5, v16, v5, 7 bitop3:0x6c
	v_mul_lo_u32 v6, v6, s68
	v_ashrrev_i32_e32 v9, 4, v168
	v_lshl_add_u32 v6, v5, 4, v6
	v_bfe_u32 v5, v168, 2, 2
	v_lshrrev_b32_e32 v7, 1, v168
	v_and_b32_e32 v10, 0x1ffff0, v9
	v_lshrrev_b32_e32 v9, 1, v9
	v_ashrrev_i32_e32 v3, 4, v3
	v_and_or_b32 v5, v7, 8, v5
	v_and_b32_e32 v7, 0x60, v168
	v_lshlrev_b32_e32 v8, 3, v168
	v_and_b32_e32 v9, 4, v9
	v_and_b32_e32 v11, 0x1ffff0, v3
	v_lshrrev_b32_e32 v3, 1, v3
	v_and_or_b32 v7, v8, 24, v7
	v_or3_b32 v9, v10, v9, v5
	v_and_b32_e32 v3, 4, v3
	s_barrier
	global_load_lds_dwordx4 v2, s[44:45]
	s_mov_b32 m0, s72
	v_lshlrev_b32_e32 v7, 1, v7
	v_lshlrev_b32_e32 v10, 11, v9
	v_or3_b32 v3, v11, v3, v5
	global_load_lds_dwordx4 v4, s[44:45]
	s_mov_b32 m0, s73
	v_or_b32_e32 v9, v10, v7
	v_lshlrev_b32_e32 v11, 11, v3
	global_load_lds_dwordx4 v6, s[44:45]
	s_mov_b32 m0, s64
	v_or_b32_e32 v3, v11, v7
	global_load_lds_dwordx4 v9, s[46:47]
	s_mov_b32 m0, s74
	v_lshlrev_b32_e32 v13, 1, v168
	global_load_lds_dwordx4 v3, s[46:47]
	v_lshlrev_b32_e32 v9, 4, v168
	v_and_b32_e32 v14, 32, v13
	v_or_b32_e32 v3, 32, v148
	v_and_b32_e32 v16, 0x13, v167
	v_and_b32_e32 v17, 4, v167
	v_lshl_or_b32 v16, v17, 1, v16
	v_and_b32_e32 v17, 8, v167
	v_lshrrev_b32_e32 v17, 1, v17
	v_or_b32_e32 v16, v16, v17
	v_mul_u32_u24_e32 v5, 0x180, v16
	v_lshlrev_b32_e32 v17, 3, v16
	v_and_b32_e32 v7, 0x70, v17
	v_and_b32_e32 v12, 0xc0, v9
	v_and_or_b32 v8, v8, s75, v14
	v_bitop3_b32 v172, v3, v5, v7 bitop3:0xde
	v_or_b32_e32 v3, 64, v148
	v_mul_i32_i24_e32 v15, -8, v169
	v_add3_u32 v169, v12, 0, v8
	v_and_b32_e32 v12, 0xc0, v13
	v_and_b32_e32 v13, 48, v9
	v_bitop3_b32 v173, v3, v5, v7 bitop3:0xde
	v_or_b32_e32 v3, 0x60, v148
	v_or3_b32 v8, v11, v12, v13
	v_mov_b32_e32 v9, v149
	v_bitop3_b32 v171, v148, v5, v7 bitop3:0xde
	v_bitop3_b32 v174, v3, v5, v7 bitop3:0xde
	v_mov_b32_e32 v3, v149
	v_mov_b32_e32 v5, v149
	v_mov_b32_e32 v7, v149
	v_lshl_add_u64 v[150:151], s[48:49], 0, v[8:9]
	v_mov_b32_e32 v240, v8
	v_or3_b32 v8, v10, v12, v13
	v_mov_b32_e32 v16, v149
	v_mov_b32_e32 v17, v149
	v_and_b32_e32 v170, 63, v168
	s_lshl_b32 s46, s80, 2
	v_lshl_add_u32 v168, v167, 2, s65
	v_lshl_add_u64 v[152:153], s[48:49], 0, v[8:9]
	v_mov_b32_e32 v241, v8
	v_lshl_add_u64 v[154:155], s[50:51], 0, v[6:7]
	v_mov_b32_e32 v242, v6
	v_lshl_add_u64 v[156:157], s[50:51], 0, v[4:5]
	v_mov_b32_e32 v243, v4
	v_lshl_add_u64 v[158:159], s[50:51], 0, v[2:3]
	v_mov_b32_e32 v244, v2
	s_add_u32 s94, s2, s50
	s_addc_u32 s95, s3, s51
	s_add_u32 s96, s2, s48
	s_addc_u32 s97, s3, s49
	v_add3_u32 v167, s63, v15, v167
	v_mov_b32_e32 v2, v149
	v_mov_b32_e32 v4, v149
	v_mov_b32_e32 v6, v149
	v_mov_b32_e32 v8, v149
	v_mov_b32_e32 v10, v149
	v_mov_b32_e32 v11, v149
	v_mov_b32_e32 v12, v149
	v_mov_b32_e32 v13, v149
	v_mov_b32_e32 v14, v149
	v_mov_b32_e32 v15, v149
	v_mov_b32_e32 v32, v16
	v_mov_b32_e32 v33, v17
	v_mov_b32_e32 v48, v16
	v_mov_b32_e32 v49, v17
	v_mov_b32_e32 v64, v16
	v_mov_b32_e32 v65, v17
	s_add_i32 s46, s46, 4
	v_cmp_gt_u32_e64 s[0:1], 32, v170
	v_mov_b32_e32 v176, 0
	v_mov_b32_e32 v175, 0
	v_mov_b32_e32 v210, 0
	v_mov_b32_e32 v211, 0
	v_mov_b32_e32 v212, 0
	v_mov_b32_e32 v213, 0
	v_mov_b32_e32 v214, 0
	v_mov_b32_e32 v215, 0
	v_mov_b32_e32 v216, 0
	v_mov_b32_e32 v217, 0
	v_mov_b32_e32 v218, 0
	v_mov_b32_e32 v219, 0
	v_mov_b32_e32 v220, 0
	v_mov_b32_e32 v221, 0
	v_mov_b32_e32 v222, 0
	v_mov_b32_e32 v223, 0
	v_mov_b32_e32 v224, 0
	v_mov_b32_e32 v225, 0
	s_movk_i32 s47, 0xff00
	v_mov_b32_e32 v30, v14
	v_mov_b32_e32 v31, v15
	v_mov_b32_e32 v28, v12
	v_mov_b32_e32 v29, v13
	v_mov_b32_e32 v26, v10
	v_mov_b32_e32 v27, v11
	v_mov_b32_e32 v24, v8
	v_mov_b32_e32 v25, v9
	v_mov_b32_e32 v22, v6
	v_mov_b32_e32 v23, v7
	v_mov_b32_e32 v20, v4
	v_mov_b32_e32 v21, v5
	v_mov_b32_e32 v18, v2
	v_mov_b32_e32 v19, v3
	v_mov_b32_e32 v46, v14
	v_mov_b32_e32 v47, v15
	v_mov_b32_e32 v44, v12
	v_mov_b32_e32 v45, v13
	v_mov_b32_e32 v42, v10
	v_mov_b32_e32 v43, v11
	v_mov_b32_e32 v40, v8
	v_mov_b32_e32 v41, v9
	v_mov_b32_e32 v38, v6
	v_mov_b32_e32 v39, v7
	v_mov_b32_e32 v36, v4
	v_mov_b32_e32 v37, v5
	v_mov_b32_e32 v34, v2
	v_mov_b32_e32 v35, v3
	v_mov_b32_e32 v62, v14
	v_mov_b32_e32 v63, v15
	v_mov_b32_e32 v60, v12
	v_mov_b32_e32 v61, v13
	v_mov_b32_e32 v58, v10
	v_mov_b32_e32 v59, v11
	v_mov_b32_e32 v56, v8
	v_mov_b32_e32 v57, v9
	v_mov_b32_e32 v54, v6
	v_mov_b32_e32 v55, v7
	v_mov_b32_e32 v52, v4
	v_mov_b32_e32 v53, v5
	v_mov_b32_e32 v50, v2
	v_mov_b32_e32 v51, v3

.LBB0_1220:
	s_add_u32 s0, s10, 0x2d000000
	s_addc_u32 s1, s11, 0
	s_lshl_b32 s15, s92, 4
	v_mov_b32_e32 v59, 0
	v_lshl_add_u64 v[154:155], s[2:3], 0, v[58:59]
	s_add_u32 s2, s10, 0x31000000
	s_addc_u32 s3, s11, 0
	s_add_u32 s4, s10, 0x35000000
	s_addc_u32 s5, s11, 0
	s_add_u32 s6, s10, 0x39000000
	s_addc_u32 s7, s11, 0
	s_add_u32 s8, s10, 0x3d000000
	s_addc_u32 s9, s11, 0
	s_add_u32 s10, s10, 0x41000000
	v_lshl_add_u64 v[156:157], s[12:13], 0, v[58:59]
	s_mul_i32 s12, s92, 24
	s_waitcnt vmcnt(3)
	v_mov_b32_e32 v62, v150
	v_mov_b32_e32 v63, v151
	v_mov_b32_e32 v58, v130
	v_mov_b32_e32 v59, v131
	v_mov_b32_e32 v66, v146
	v_mov_b32_e32 v67, v147
	v_mov_b32_e32 v70, v142
	v_mov_b32_e32 v71, v143
	v_mov_b32_e32 v74, v138
	v_mov_b32_e32 v75, v139
	s_waitcnt vmcnt(2)
	v_mov_b32_e32 v78, v126
	v_mov_b32_e32 v79, v127
	s_waitcnt vmcnt(1)
	v_mov_b32_e32 v82, v134
	v_mov_b32_e32 v83, v135
	s_waitcnt vmcnt(0)
	v_mov_b32_e32 v86, v122
	v_mov_b32_e32 v87, v123
	s_addc_u32 s11, s11, 0
	s_add_i32 s16, s14, s90
	s_add_i32 s17, s14, s12
	s_add_i32 s18, s14, s15
	s_mov_b32 s19, 0xbfb8aa3b
	s_mov_b32 s20, 0x179abe15
	v_mov_b32_e32 v158, 0x2200
	v_mov_b32_e32 v159, 0x1800
	v_mov_b32_e32 v160, 0x5368d4a5
	v_readlane_b32 s21, v254, 2
	v_mov_b32_e32 v64, v152
	v_mov_b32_e32 v65, v153
	v_mov_b32_e32 v60, v132
	v_mov_b32_e32 v61, v133
	v_mov_b32_e32 v68, v148
	v_mov_b32_e32 v69, v149
	v_mov_b32_e32 v72, v144
	v_mov_b32_e32 v73, v145
	v_mov_b32_e32 v76, v140
	v_mov_b32_e32 v77, v141
	v_mov_b32_e32 v80, v128
	v_mov_b32_e32 v81, v129
	v_mov_b32_e32 v84, v136
	v_mov_b32_e32 v85, v137
	v_mov_b32_e32 v88, v124
	v_mov_b32_e32 v89, v125
	s_branch .LBB0_1223
.LBB0_1221:
	s_ashr_i32 s12, s13, 1
	s_and_b32 s13, s13, 0x3ffe
	s_cmp_eq_u32 s13, 0
	v_lshlrev_b32_e32 v164, 16, v110
	v_and_b32_e32 v165, 0xffff0000, v110
	v_lshlrev_b32_e32 v173, 16, v111
	v_and_b32_e32 v174, 0xffff0000, v111
	s_cselect_b64 s[22:23], -1, 0
	v_lshlrev_b32_e32 v161, 16, v118
	v_and_b32_e32 v166, 0xffff0000, v118
	v_lshlrev_b32_e32 v167, 16, v119
	v_and_b32_e32 v168, 0xffff0000, v119
	v_lshlrev_b32_e32 v118, 16, v114
	v_and_b32_e32 v119, 0xffff0000, v114
	v_lshlrev_b32_e32 v114, 16, v115
	v_and_b32_e32 v115, 0xffff0000, v115
	v_lshlrev_b32_e32 v175, 16, v112
	v_and_b32_e32 v176, 0xffff0000, v112
	v_lshlrev_b32_e32 v177, 16, v113
	v_and_b32_e32 v178, 0xffff0000, v113
	v_lshlrev_b32_e32 v112, 16, v98
	v_and_b32_e32 v113, 0xffff0000, v98
	v_lshlrev_b32_e32 v98, 16, v106
	v_and_b32_e32 v179, 0xffff0000, v106
	v_lshlrev_b32_e32 v180, 16, v107
	v_and_b32_e32 v181, 0xffff0000, v107
	v_lshlrev_b32_e32 v162, 16, v100
	v_and_b32_e32 v163, 0xffff0000, v100
	v_lshlrev_b32_e32 v106, 16, v101
	v_and_b32_e32 v107, 0xffff0000, v101
	v_lshlrev_b32_e32 v183, 16, v109
	v_and_b32_e32 v184, 0xffff0000, v109
	v_lshlrev_b32_e32 v100, 16, v94
	v_and_b32_e32 v101, 0xffff0000, v94
	v_lshlrev_b32_e32 v109, 16, v95
	v_and_b32_e32 v185, 0xffff0000, v95
	v_lshlrev_b32_e32 v186, 16, v96
	v_and_b32_e32 v187, 0xffff0000, v96
	v_lshlrev_b32_e32 v188, 16, v97
	v_and_b32_e32 v189, 0xffff0000, v97
	v_cndmask_b32_e64 v95, v165, 0, s[22:23]
	v_cndmask_b32_e64 v94, v164, 0, s[22:23]
	v_cndmask_b32_e64 v97, v174, 0, s[22:23]
	v_cndmask_b32_e64 v96, v173, 0, s[22:23]
	v_add_f32_e64 v94, v94, -v118
	v_add_f32_e64 v95, v95, -v119
	v_add_f32_e64 v96, v96, -v114
	v_add_f32_e64 v97, v97, -v115
	v_lshlrev_b32_e32 v169, 16, v120
	v_and_b32_e32 v170, 0xffff0000, v120
	v_lshlrev_b32_e32 v171, 16, v121
	v_and_b32_e32 v172, 0xffff0000, v121
	v_lshlrev_b32_e32 v120, 16, v116
	v_and_b32_e32 v121, 0xffff0000, v116
	v_lshlrev_b32_e32 v190, 16, v102
	v_and_b32_e32 v191, 0xffff0000, v102
	v_lshlrev_b32_e32 v192, 16, v103
	v_and_b32_e32 v193, 0xffff0000, v103
	v_lshlrev_b32_e32 v198, 16, v90
	v_and_b32_e32 v199, 0xffff0000, v90
	v_cndmask_b32_e64 v103, v176, 0, s[22:23]
	v_cndmask_b32_e64 v102, v175, 0, s[22:23]
	v_fma_f32 v94, v22, v94, v118
	v_fma_f32 v95, v23, v95, v119
	v_fma_f32 v96, v24, v96, v114
	v_fma_f32 v97, v25, v97, v115
	v_cvt_pk_f16_f32 v94, v94, v95
	v_cvt_pk_f16_f32 v95, v96, v97
	v_add_f32_e64 v96, v102, -v120
	v_add_f32_e64 v97, v103, -v121
	v_add_f32_e32 v102, v6, v198
	v_add_f32_e32 v103, v7, v199
	v_mul_f32_e32 v102, 0xbfb8aa3b, v102
	v_mul_f32_e32 v103, 0xbfb8aa3b, v103
	v_exp_f32_e32 v102, v102
	v_exp_f32_e32 v103, v103
	v_lshlrev_b32_e32 v200, 16, v91
	v_fma_f32 v96, v14, v96, v120
	v_fma_f32 v97, v15, v97, v121
	v_and_b32_e32 v201, 0xffff0000, v91
	v_cvt_pk_f16_f32 v96, v96, v97
	v_add_f32_e32 v97, v8, v200
	v_add_f32_e32 v102, 1.0, v102
	v_add_f32_e32 v103, 1.0, v103
	v_mul_f32_e32 v97, 0xbfb8aa3b, v97
	v_add_f32_e32 v114, v9, v201
	v_rcp_f32_e32 v102, v102
	v_rcp_f32_e32 v103, v103
	v_exp_f32_e32 v97, v97
	v_mul_f32_e32 v114, 0xbfb8aa3b, v114
	v_exp_f32_e32 v115, v114
	v_lshlrev_b32_e32 v110, 16, v117
	v_and_b32_e32 v111, 0xffff0000, v117
	v_lshlrev_b32_e32 v116, 16, v99
	v_and_b32_e32 v117, 0xffff0000, v99
	v_cndmask_b32_e64 v99, v179, 0, s[22:23]
	v_cndmask_b32_e64 v98, v98, 0, s[22:23]
	v_add_f32_e64 v98, v98, -v112
	v_add_f32_e64 v99, v99, -v113
	v_add_f32_e32 v97, 1.0, v97
	v_fma_f32 v112, v30, v98, v112
	v_fma_f32 v113, v31, v99, v113
	v_add_f32_e64 v98, v102, -1.0
	v_add_f32_e64 v99, v103, -1.0
	v_lshlrev_b32_e32 v202, 16, v92
	v_fma_f32 v98, v54, v98, 1.0
	v_fma_f32 v99, v55, v99, 1.0
	v_rcp_f32_e32 v114, v97
	v_add_f32_e32 v97, 1.0, v115
	v_and_b32_e32 v203, 0xffff0000, v92
	v_mul_f32_e32 v98, v98, v112
	v_mul_f32_e32 v99, v99, v113
	v_rcp_f32_e32 v115, v97
	v_add_f32_e32 v97, v2, v202
	v_cvt_pk_f16_f32 v98, v98, v99
	v_mul_f32_e32 v97, 0xbfb8aa3b, v97
	v_add_f32_e32 v99, v3, v203
	v_exp_f32_e32 v97, v97
	v_mul_f32_e32 v99, 0xbfb8aa3b, v99
	v_exp_f32_e32 v99, v99
	v_cndmask_b32_e64 v90, v100, 0, s[22:23]
	v_cndmask_b32_e64 v91, v101, 0, s[22:23]
	v_cndmask_b32_e64 v101, v181, 0, s[22:23]
	v_cndmask_b32_e64 v100, v180, 0, s[22:23]
	v_add_f32_e32 v97, 1.0, v97
	v_add_f32_e64 v100, v100, -v116
	v_add_f32_e64 v101, v101, -v117
	v_rcp_f32_e32 v118, v97
	v_add_f32_e32 v97, 1.0, v99
	v_fma_f32 v116, v32, v100, v116
	v_fma_f32 v117, v33, v101, v117
	v_add_f32_e64 v100, v114, -1.0
	v_add_f32_e64 v101, v115, -1.0
	v_rcp_f32_e32 v119, v97
	v_lshlrev_b32_e32 v182, 16, v108
	v_and_b32_e32 v108, 0xffff0000, v108
	v_fma_f32 v100, v56, v100, 1.0
	v_fma_f32 v101, v57, v101, 1.0
	v_add_f32_e32 v121, v18, v190
	v_lshlrev_b32_e32 v194, 16, v104
	v_and_b32_e32 v195, 0xffff0000, v104
	v_lshlrev_b32_e32 v196, 16, v105
	v_and_b32_e32 v197, 0xffff0000, v105
	v_cndmask_b32_e64 v105, v108, 0, s[22:23]
	v_cndmask_b32_e64 v104, v182, 0, s[22:23]
	v_mul_f32_e32 v100, v100, v116
	v_mul_f32_e32 v101, v101, v117
	v_mul_f32_e64 v120, |v121|, s19
	v_lshlrev_b32_e32 v204, 16, v93
	v_cvt_pk_f16_f32 v99, v100, v101
	v_add_f32_e64 v100, v104, -v162
	v_add_f32_e64 v101, v105, -v163
	v_exp_f32_e32 v120, v120
	v_fma_f32 v104, v38, v100, v162
	v_fma_f32 v105, v39, v101, v163
	v_add_f32_e64 v100, v118, -1.0
	v_add_f32_e64 v101, v119, -1.0
	v_add_f32_e32 v97, v4, v204
	v_fma_f32 v100, v46, v100, 1.0
	v_fma_f32 v101, v47, v101, 1.0
	v_mul_f32_e32 v97, 0xbfb8aa3b, v97
	v_mul_f32_e32 v100, v100, v104
	v_mul_f32_e32 v101, v101, v105
	v_exp_f32_e32 v97, v97
	v_cvt_pk_f16_f32 v100, v100, v101
	v_add_f32_e32 v101, 1.0, v120
	v_log_f32_e32 v101, v101
	v_add_f32_e32 v97, 1.0, v97
	v_rcp_f32_e32 v120, v97
	v_max_f32_e64 v97, -v121, 0
	v_fmac_f32_e32 v97, 0x3f317218, v101
	v_add_f32_e32 v101, v19, v191
	v_mul_f32_e64 v121, |v101|, s19
	v_exp_f32_e32 v121, v121
	v_cndmask_b32_e64 v92, v109, 0, s[22:23]
	v_sub_f32_e32 v90, v90, v161
	v_and_b32_e32 v205, 0xffff0000, v93
	v_cndmask_b32_e64 v93, v185, 0, s[22:23]
	v_cndmask_b32_e64 v175, v188, 0, s[22:23]
	v_fma_mixlo_f16 v90, v26, v90, v161
	v_sub_f32_e32 v161, v91, v166
	v_sub_f32_e32 v91, v92, v167
	v_sub_f32_e32 v97, -0.5, v97
	v_fma_mixlo_f16 v91, v28, v91, v167
	v_sub_f32_e32 v167, v93, v168
	v_sub_f32_e32 v93, v175, v171
	v_mul_f32_e32 v97, 0x3fb8aa3b, v97
	v_fma_mixlo_f16 v93, v36, v93, v171
	v_exp_f32_e32 v171, v97
	v_add_f32_e32 v97, 1.0, v121
	v_add_f32_e32 v121, v20, v192
	v_log_f32_e32 v97, v97
	v_mul_f32_e64 v162, |v121|, s19
	v_exp_f32_e32 v162, v162
	v_max_f32_e64 v101, -v101, 0
	v_fmac_f32_e32 v101, 0x3f317218, v97
	v_sub_f32_e32 v97, -0.5, v101
	v_add_f32_e32 v101, 1.0, v162
	v_log_f32_e32 v101, v101
	v_cndmask_b32_e64 v173, v186, 0, s[22:23]
	v_mul_f32_e32 v97, 0x3fb8aa3b, v97
	v_sub_f32_e32 v92, v173, v169
	v_exp_f32_e32 v173, v97
	v_max_f32_e64 v97, -v121, 0
	v_fmac_f32_e32 v97, 0x3f317218, v101
	v_add_f32_e32 v101, v21, v193
	v_mul_f32_e64 v121, |v101|, s19
	v_exp_f32_e32 v121, v121
	v_sub_f32_e32 v97, -0.5, v97
	v_cndmask_b32_e64 v174, v187, 0, s[22:23]
	v_mul_f32_e32 v97, 0x3fb8aa3b, v97
	v_fma_mixlo_f16 v92, v34, v92, v169
	v_sub_f32_e32 v169, v174, v170
	v_exp_f32_e32 v174, v97
	v_add_f32_e32 v97, 1.0, v121
	v_add_f32_e32 v121, v10, v194
	v_log_f32_e32 v97, v97
	v_mul_f32_e64 v162, |v121|, s19
	v_exp_f32_e32 v162, v162
	v_max_f32_e64 v101, -v101, 0
	v_fmac_f32_e32 v101, 0x3f317218, v97
	v_sub_f32_e32 v97, -0.5, v101
	v_add_f32_e32 v101, 1.0, v162
	v_log_f32_e32 v101, v101
	v_mul_f32_e32 v97, 0x3fb8aa3b, v97
	v_exp_f32_e32 v175, v97
	v_max_f32_e64 v97, -v121, 0
	v_fmac_f32_e32 v97, 0x3f317218, v101
	v_add_f32_e32 v101, v11, v195
	v_mul_f32_e64 v121, |v101|, s19
	v_exp_f32_e32 v121, v121
	v_sub_f32_e32 v97, -0.5, v97
	v_mul_f32_e32 v97, 0x3fb8aa3b, v97
	v_cndmask_b32_e64 v108, v177, 0, s[22:23]
	v_exp_f32_e32 v177, v97
	v_add_f32_e32 v97, 1.0, v121
	v_add_f32_e32 v121, v12, v196
	v_log_f32_e32 v97, v97
	v_mul_f32_e64 v162, |v121|, s19
	v_exp_f32_e32 v162, v162
	v_max_f32_e64 v101, -v101, 0
	v_fmac_f32_e32 v101, 0x3f317218, v97
	v_sub_f32_e32 v97, -0.5, v101
	v_add_f32_e32 v101, 1.0, v162
	v_log_f32_e32 v101, v101
	v_mul_f32_e32 v97, 0x3fb8aa3b, v97
	v_cndmask_b32_e64 v109, v178, 0, s[22:23]
	v_exp_f32_e32 v178, v97
	v_max_f32_e64 v97, -v121, 0
	v_fmac_f32_e32 v97, 0x3f317218, v101
	v_add_f32_e32 v101, v13, v197
	v_mul_f32_e64 v121, |v101|, s19
	v_exp_f32_e32 v121, v121
	v_sub_f32_e32 v97, -0.5, v97
	v_mul_f32_e32 v97, 0x3fb8aa3b, v97
	v_exp_f32_e32 v179, v97
	v_max_f32_e64 v97, -v101, 0
	v_add_f32_e32 v101, 1.0, v121
	v_add_f32_e32 v121, v5, v205
	v_mul_f32_e32 v121, 0xbfb8aa3b, v121
	v_log_f32_e32 v101, v101
	v_exp_f32_e32 v121, v121
	v_add_f32_e64 v108, v108, -v110
	v_add_f32_e64 v109, v109, -v111
	v_cndmask_b32_e64 v165, v184, 0, s[22:23]
	v_fmac_f32_e32 v97, 0x3f317218, v101
	v_add_f32_e32 v101, 1.0, v121
	v_rcp_f32_e32 v121, v101
	v_sub_f32_e32 v97, -0.5, v97
	v_cndmask_b32_e64 v164, v183, 0, s[22:23]
	v_mul_f32_e32 v97, 0x3fb8aa3b, v97
	v_fma_f32 v108, v16, v108, v110
	v_fma_f32 v109, v17, v109, v111
	v_exp_f32_e32 v180, v97
	v_add_f32_e64 v162, v164, -v106
	v_add_f32_e64 v163, v165, -v107
	v_cvt_pk_f16_f32 v97, v108, v109
	v_mul_f32_e32 v108, v50, v112
	v_mul_f32_e32 v109, v51, v113
	v_fma_f32 v106, v40, v162, v106
	v_fma_f32 v107, v41, v163, v107
	v_add_f32_e64 v162, v120, -1.0
	v_add_f32_e64 v163, v121, -1.0
	v_mul_f32_e32 v110, v108, v108
	v_mul_f32_e32 v111, v109, v109
	v_mul_f32_e32 v112, v52, v116
	v_mul_f32_e32 v113, v53, v117
	v_fma_f32 v162, v48, v162, 1.0
	v_fma_f32 v163, v49, v163, 1.0
	v_mul_f32_e32 v116, v112, v112
	v_mul_f32_e32 v117, v113, v113
	v_add_f32_e32 v110, v110, v111
	v_mul_f32_e32 v162, v162, v106
	v_mul_f32_e32 v163, v163, v107
	v_mul_f32_e32 v104, v42, v104
	v_mul_f32_e32 v105, v43, v105
	v_add_f32_e32 v110, v116, v110
	v_cvt_pk_f16_f32 v101, v162, v163
	v_mul_f32_e32 v162, v104, v104
	v_mul_f32_e32 v163, v105, v105
	v_add_f32_e32 v110, v117, v110
	v_mul_f32_e32 v106, v44, v106
	v_mul_f32_e32 v107, v45, v107
	v_add_f32_e32 v110, v162, v110
	v_mul_f32_e32 v164, v106, v106
	v_mul_f32_e32 v165, v107, v107
	v_add_f32_e32 v110, v163, v110
	v_add_f32_e32 v110, v164, v110
	v_add_f32_e32 v110, v165, v110
	s_ashr_i32 s13, s12, 31
	s_lshl_b64 s[12:13], s[12:13], 11
	v_add_f32_dpp v110, v110, v110 quad_perm:[1,0,3,2] row_mask:0xf bank_mask:0xf bound_ctrl:1
	v_cndmask_b32_e64 v176, v189, 0, s[22:23]
	v_sub_f32_e32 v176, v176, v172
	v_add_f32_dpp v110, v110, v110 quad_perm:[2,3,0,1] row_mask:0xf bank_mask:0xf bound_ctrl:1
	v_fma_mixhi_f16 v93, v37, v176, v172
	v_fma_mixhi_f16 v92, v35, v169, v170
	v_add_f32_dpp v110, v110, v110 row_half_mirror row_mask:0xf bank_mask:0xf bound_ctrl:1
	v_rsq_f32_e32 v111, v110
	v_cmp_lt_f32_e32 vcc, s20, v110
	v_fma_mixhi_f16 v91, v29, v167, v168
	v_fma_mixhi_f16 v90, v27, v161, v166
	v_cndmask_b32_e32 v110, v160, v111, vcc
	v_mul_f32_e32 v116, v108, v110
	v_mul_f32_e32 v117, v109, v110
	v_mul_f32_e32 v112, v112, v110
	v_mul_f32_e32 v113, v113, v110
	v_mul_f32_e32 v102, v102, v116
	v_mul_f32_e32 v103, v103, v117
	v_mul_f32_e32 v108, v114, v112
	v_mul_f32_e32 v109, v115, v113
	v_mul_f32_e32 v114, v104, v110
	v_mul_f32_e32 v115, v105, v110
	v_mul_f32_e32 v106, v106, v110
	v_mul_f32_e32 v107, v107, v110
	v_cvt_pk_f16_f32 v102, v102, v103
	v_cvt_pk_f16_f32 v103, v108, v109
	v_mul_f32_e32 v104, v118, v114
	v_mul_f32_e32 v105, v119, v115
	v_mul_f32_e32 v108, v120, v106
	v_mul_f32_e32 v109, v121, v107
	v_cvt_pk_f16_f32 v104, v104, v105
	v_cvt_pk_f16_f32 v105, v108, v109
	v_cvt_pk_f16_f32 v108, v114, v115
	v_lshl_or_b32 v114, v1, 1, s12
	v_mov_b32_e32 v115, s13
	v_cvt_pk_f16_f32 v109, v106, v107
	v_cvt_pk_f16_f32 v107, v112, v113
	v_cvt_pk_f16_f32 v106, v116, v117
	v_cvt_pk_f16_f32 v113, -v179, -v180
	v_cvt_pk_f16_f32 v112, -v177, -v178
	v_cvt_pk_f16_f32 v111, -v174, -v175
	v_cvt_pk_f16_f32 v110, -v171, -v173
	v_lshl_add_u64 v[116:117], s[0:1], 0, v[114:115]
	global_store_dwordx4 v[116:117], v[110:113], off
	s_waitcnt vmcnt(7)
	v_mov_b32_e32 v118, v130
	v_mov_b32_e32 v119, v131
	v_mov_b32_e32 v120, v132
	v_mov_b32_e32 v121, v133
	v_lshl_add_u64 v[110:111], s[2:3], 0, v[114:115]
	global_store_dwordx4 v[110:111], v[106:109], off
	s_waitcnt vmcnt(6)
	v_mov_b32_e32 v110, v134
	v_mov_b32_e32 v111, v135
	v_mov_b32_e32 v112, v136
	v_mov_b32_e32 v113, v137
	v_lshl_add_u64 v[106:107], s[4:5], 0, v[114:115]
	global_store_dwordx4 v[106:107], v[102:105], off
	s_waitcnt vmcnt(6)
	v_mov_b32_e32 v106, v138
	v_mov_b32_e32 v107, v139
	v_mov_b32_e32 v108, v140
	v_mov_b32_e32 v109, v141
	v_lshl_add_u64 v[102:103], s[6:7], 0, v[114:115]
	global_store_dwordx4 v[102:103], v[98:101], off
	s_waitcnt vmcnt(5)
	v_mov_b32_e32 v102, v146
	v_mov_b32_e32 v103, v147
	v_mov_b32_e32 v104, v148
	v_mov_b32_e32 v105, v149
	v_lshl_add_u64 v[98:99], s[8:9], 0, v[114:115]
	global_store_dwordx4 v[98:99], v[94:97], off
	v_mov_b32_e32 v98, v126
	v_mov_b32_e32 v99, v127
	v_mov_b32_e32 v100, v128
	v_mov_b32_e32 v101, v129
	v_lshl_add_u64 v[94:95], s[10:11], 0, v[114:115]
	global_store_dwordx4 v[94:95], v[90:93], off
	v_mov_b32_e32 v94, v142
	v_mov_b32_e32 v95, v143
	v_mov_b32_e32 v114, v122
	v_mov_b32_e32 v115, v123
	s_waitcnt vmcnt(6)
	v_mov_b32_e32 v90, v150
	v_mov_b32_e32 v91, v151
	v_mov_b32_e32 v92, v152
	v_mov_b32_e32 v93, v153
	v_mov_b32_e32 v96, v144
	v_mov_b32_e32 v97, v145
	v_mov_b32_e32 v116, v124
	v_mov_b32_e32 v117, v125
.LBB0_1222:
	s_add_i32 s21, s21, s15
	s_add_i32 s12, s14, s21
	s_waitcnt vmcnt(6)
	v_mov_b32_e32 v124, v88
	v_mov_b32_e32 v125, v89
	v_mov_b32_e32 v136, v84
	v_mov_b32_e32 v137, v85
	v_mov_b32_e32 v128, v80
	v_mov_b32_e32 v129, v81
	v_mov_b32_e32 v140, v76
	v_mov_b32_e32 v141, v77
	v_mov_b32_e32 v144, v72
	v_mov_b32_e32 v145, v73
	v_mov_b32_e32 v148, v68
	v_mov_b32_e32 v149, v69
	v_mov_b32_e32 v132, v60
	v_mov_b32_e32 v133, v61
	v_mov_b32_e32 v152, v64
	v_mov_b32_e32 v153, v65
	s_cmp_lt_i32 s12, 0x10000
	v_mov_b32_e32 v122, v86
	v_mov_b32_e32 v123, v87
	v_mov_b32_e32 v134, v82
	v_mov_b32_e32 v135, v83
	v_mov_b32_e32 v126, v78
	v_mov_b32_e32 v127, v79
	v_mov_b32_e32 v138, v74
	v_mov_b32_e32 v139, v75
	v_mov_b32_e32 v142, v70
	v_mov_b32_e32 v143, v71
	v_mov_b32_e32 v146, v66
	v_mov_b32_e32 v147, v67
	v_mov_b32_e32 v130, v58
	v_mov_b32_e32 v131, v59
	v_mov_b32_e32 v150, v62
	v_mov_b32_e32 v151, v63
	s_cbranch_scc0 .LBB0_1228

.LBB0_1225:
	s_add_i32 s13, s14, s21
	s_ashr_i32 s12, s13, 1
	s_and_b32 s13, s13, 0x3ffe
	s_cmp_eq_u32 s13, 0
	v_lshlrev_b32_e32 v175, 16, v144
	v_and_b32_e32 v176, 0xffff0000, v144
	v_lshlrev_b32_e32 v182, 16, v140
	v_and_b32_e32 v140, 0xffff0000, v140
	v_lshlrev_b32_e32 v184, 16, v127
	v_and_b32_e32 v127, 0xffff0000, v127
	v_lshlrev_b32_e32 v185, 16, v128
	v_and_b32_e32 v128, 0xffff0000, v128
	v_lshlrev_b32_e32 v186, 16, v129
	s_cselect_b64 s[22:23], -1, 0
	v_lshlrev_b32_e32 v161, 16, v150
	v_and_b32_e32 v166, 0xffff0000, v150
	v_lshlrev_b32_e32 v150, 16, v151
	v_and_b32_e32 v167, 0xffff0000, v151
	v_lshlrev_b32_e32 v151, 16, v152
	v_and_b32_e32 v168, 0xffff0000, v152
	v_lshlrev_b32_e32 v152, 16, v153
	v_and_b32_e32 v169, 0xffff0000, v153
	v_lshlrev_b32_e32 v153, 16, v146
	v_and_b32_e32 v170, 0xffff0000, v146
	v_lshlrev_b32_e32 v162, 16, v147
	v_and_b32_e32 v171, 0xffff0000, v147
	v_lshlrev_b32_e32 v163, 16, v148
	v_and_b32_e32 v172, 0xffff0000, v148
	v_lshlrev_b32_e32 v148, 16, v149
	v_lshlrev_b32_e32 v180, 16, v139
	v_lshlrev_b32_e32 v146, 16, v132
	v_and_b32_e32 v147, 0xffff0000, v132
	v_lshlrev_b32_e32 v183, 16, v141
	v_and_b32_e32 v141, 0xffff0000, v141
	v_lshlrev_b32_e32 v132, 16, v126
	v_lshlrev_b32_e32 v189, 16, v135
	v_and_b32_e32 v190, 0xffff0000, v135
	v_lshlrev_b32_e32 v195, 16, v122
	v_and_b32_e32 v196, 0xffff0000, v122
	v_lshlrev_b32_e32 v201, 16, v125
	v_and_b32_e32 v202, 0xffff0000, v125
	v_cndmask_b32_e64 v125, v127, 0, s[22:23]
	v_cndmask_b32_e64 v175, v175, 0, s[22:23]
	v_cndmask_b32_e64 v135, v140, 0, s[22:23]
	v_cndmask_b32_e64 v140, v176, 0, s[22:23]
	v_cndmask_b32_e64 v127, v128, 0, s[22:23]
	v_cndmask_b32_e64 v128, v186, 0, s[22:23]
	v_lshlrev_b32_e32 v193, 16, v137
	v_and_b32_e32 v194, 0xffff0000, v137
	v_cndmask_b32_e64 v122, v132, 0, s[22:23]
	v_cndmask_b32_e64 v132, v180, 0, s[22:23]
	v_cndmask_b32_e64 v137, v141, 0, s[22:23]
	v_sub_f32_e32 v180, v125, v171
	v_sub_f32_e32 v125, v128, v148
	v_sub_f32_e32 v128, v175, v151
	v_sub_f32_e32 v175, v140, v168
	v_add_f32_e32 v140, v6, v195
	v_add_f32_e32 v141, v7, v196
	v_mul_f32_e32 v140, 0xbfb8aa3b, v140
	v_mul_f32_e32 v141, 0xbfb8aa3b, v141
	v_exp_f32_e32 v140, v140
	v_exp_f32_e32 v141, v141
	v_and_b32_e32 v173, 0xffff0000, v149
	v_lshlrev_b32_e32 v149, 16, v142
	v_and_b32_e32 v126, 0xffff0000, v126
	v_add_f32_e32 v140, 1.0, v140
	v_add_f32_e32 v141, 1.0, v141
	v_and_b32_e32 v179, 0xffff0000, v138
	v_lshlrev_b32_e32 v197, 16, v123
	v_and_b32_e32 v198, 0xffff0000, v123
	v_lshlrev_b32_e32 v199, 16, v124
	v_and_b32_e32 v200, 0xffff0000, v124
	v_cndmask_b32_e64 v149, v149, 0, s[22:23]
	v_cndmask_b32_e64 v123, v126, 0, s[22:23]
	v_cndmask_b32_e64 v124, v184, 0, s[22:23]
	v_cndmask_b32_e64 v126, v185, 0, s[22:23]
	v_rcp_f32_e32 v140, v140
	v_rcp_f32_e32 v141, v141
	v_and_b32_e32 v164, 0xffff0000, v142
	v_lshlrev_b32_e32 v165, 16, v143
	v_and_b32_e32 v174, 0xffff0000, v143
	v_lshlrev_b32_e32 v177, 16, v145
	v_and_b32_e32 v178, 0xffff0000, v145
	v_lshlrev_b32_e32 v142, 16, v130
	v_and_b32_e32 v143, 0xffff0000, v130
	v_lshlrev_b32_e32 v130, 16, v138
	v_lshlrev_b32_e32 v144, 16, v131
	v_and_b32_e32 v145, 0xffff0000, v131
	v_cndmask_b32_e64 v131, v179, 0, s[22:23]
	v_sub_f32_e32 v179, v123, v170
	v_sub_f32_e32 v123, v124, v162
	v_sub_f32_e32 v124, v126, v163
	v_fma_mixlo_f16 v125, v36, v125, v148
	v_sub_f32_e32 v126, v149, v161
	v_add_f32_e32 v148, v8, v197
	v_add_f32_e32 v149, v9, v198
	v_cndmask_b32_e64 v130, v130, 0, s[22:23]
	v_mul_f32_e32 v148, 0xbfb8aa3b, v148
	v_mul_f32_e32 v149, 0xbfb8aa3b, v149
	v_add_f32_e64 v130, v130, -v142
	v_add_f32_e64 v131, v131, -v143
	v_exp_f32_e32 v148, v148
	v_exp_f32_e32 v149, v149
	v_fma_f32 v142, v30, v130, v142
	v_fma_f32 v143, v31, v131, v143
	v_add_f32_e64 v130, v140, -1.0
	v_add_f32_e64 v131, v141, -1.0
	v_and_b32_e32 v181, 0xffff0000, v139
	v_fma_f32 v130, v54, v130, 1.0
	v_fma_f32 v131, v55, v131, 1.0
	v_cndmask_b32_e64 v165, v165, 0, s[22:23]
	v_mul_f32_e32 v130, v130, v142
	v_mul_f32_e32 v131, v131, v143
	v_lshlrev_b32_e32 v138, 16, v133
	v_and_b32_e32 v139, 0xffff0000, v133
	v_cndmask_b32_e64 v133, v181, 0, s[22:23]
	v_sub_f32_e32 v181, v127, v172
	v_sub_f32_e32 v127, v165, v150
	v_add_f32_e32 v148, 1.0, v148
	v_add_f32_e32 v149, 1.0, v149
	v_cvt_pk_f16_f32 v130, v130, v131
	v_add_f32_e32 v131, v2, v199
	v_fma_mixlo_f16 v127, v24, v127, v150
	v_rcp_f32_e32 v148, v148
	v_rcp_f32_e32 v149, v149
	v_mul_f32_e32 v131, 0xbfb8aa3b, v131
	v_add_f32_e32 v150, v3, v200
	v_exp_f32_e32 v131, v131
	v_mul_f32_e32 v150, 0xbfb8aa3b, v150
	v_fma_mixlo_f16 v128, v14, v128, v151
	v_exp_f32_e32 v151, v150
	v_add_f32_e64 v132, v132, -v144
	v_add_f32_e64 v133, v133, -v145
	v_add_f32_e32 v131, 1.0, v131
	v_fma_f32 v144, v32, v132, v144
	v_fma_f32 v145, v33, v133, v145
	v_add_f32_e64 v132, v148, -1.0
	v_add_f32_e64 v133, v149, -1.0
	v_lshlrev_b32_e32 v187, 16, v134
	v_fma_f32 v132, v56, v132, 1.0
	v_fma_f32 v133, v57, v133, 1.0
	v_and_b32_e32 v188, 0xffff0000, v134
	v_cndmask_b32_e64 v134, v182, 0, s[22:23]
	v_mul_f32_e32 v132, v132, v144
	v_mul_f32_e32 v133, v133, v145
	v_rcp_f32_e32 v150, v131
	v_add_f32_e32 v131, 1.0, v151
	v_and_b32_e32 v129, 0xffff0000, v129
	v_cndmask_b32_e64 v176, v177, 0, s[22:23]
	v_rcp_f32_e32 v151, v131
	v_cvt_pk_f16_f32 v131, v132, v133
	v_add_f32_e64 v132, v134, -v146
	v_add_f32_e64 v133, v135, -v147
	v_cndmask_b32_e64 v177, v178, 0, s[22:23]
	v_cndmask_b32_e64 v178, v129, 0, s[22:23]
	v_sub_f32_e32 v129, v176, v152
	v_fma_f32 v134, v38, v132, v146
	v_fma_f32 v135, v39, v133, v147
	v_add_f32_e32 v147, v18, v187
	v_fma_mixlo_f16 v129, v16, v129, v152
	v_mul_f32_e64 v152, |v147|, s19
	v_exp_f32_e32 v152, v152
	v_add_f32_e64 v132, v150, -1.0
	v_add_f32_e64 v133, v151, -1.0
	v_max_f32_e64 v147, -v147, 0
	v_fma_f32 v132, v46, v132, 1.0
	v_fma_f32 v133, v47, v133, 1.0
	v_sub_f32_e32 v122, v122, v153
	v_mul_f32_e32 v132, v132, v134
	v_mul_f32_e32 v133, v133, v135
	v_fma_mixlo_f16 v122, v26, v122, v153
	v_cvt_pk_f16_f32 v132, v132, v133
	v_add_f32_e32 v133, 1.0, v152
	v_log_f32_e32 v133, v133
	v_lshlrev_b32_e32 v191, 16, v136
	v_and_b32_e32 v192, 0xffff0000, v136
	v_cndmask_b32_e64 v136, v183, 0, s[22:23]
	v_fmac_f32_e32 v147, 0x3f317218, v133
	v_add_f32_e32 v133, v19, v188
	v_mul_f32_e64 v152, |v133|, s19
	v_exp_f32_e32 v152, v152
	v_sub_f32_e32 v147, -0.5, v147
	v_mul_f32_e32 v147, 0x3fb8aa3b, v147
	v_exp_f32_e32 v176, v147
	v_add_f32_e32 v147, 1.0, v152
	v_add_f32_e32 v152, v20, v189
	v_mul_f32_e64 v153, |v152|, s19
	v_log_f32_e32 v147, v147
	v_exp_f32_e32 v153, v153
	v_max_f32_e64 v133, -v133, 0
	v_add_f32_e32 v146, v4, v201
	v_fmac_f32_e32 v133, 0x3f317218, v147
	v_add_f32_e32 v147, 1.0, v153
	v_log_f32_e32 v147, v147
	v_sub_f32_e32 v133, -0.5, v133
	v_mul_f32_e32 v133, 0x3fb8aa3b, v133
	v_exp_f32_e32 v182, v133
	v_max_f32_e64 v133, -v152, 0
	v_fmac_f32_e32 v133, 0x3f317218, v147
	v_add_f32_e32 v147, v21, v190
	v_mul_f32_e64 v152, |v147|, s19
	v_exp_f32_e32 v152, v152
	v_sub_f32_e32 v133, -0.5, v133
	v_mul_f32_e32 v133, 0x3fb8aa3b, v133
	v_exp_f32_e32 v183, v133
	v_add_f32_e32 v133, 1.0, v152
	v_add_f32_e32 v152, v10, v191
	v_log_f32_e32 v133, v133
	v_mul_f32_e64 v153, |v152|, s19
	v_exp_f32_e32 v153, v153
	v_max_f32_e64 v147, -v147, 0
	v_fmac_f32_e32 v147, 0x3f317218, v133
	v_sub_f32_e32 v133, -0.5, v147
	v_add_f32_e32 v147, 1.0, v153
	v_log_f32_e32 v147, v147
	v_mul_f32_e32 v133, 0x3fb8aa3b, v133
	v_exp_f32_e32 v184, v133
	v_max_f32_e64 v133, -v152, 0
	v_fmac_f32_e32 v133, 0x3f317218, v147
	v_add_f32_e32 v147, v11, v192
	v_mul_f32_e64 v152, |v147|, s19
	v_exp_f32_e32 v152, v152
	v_sub_f32_e32 v133, -0.5, v133
	v_mul_f32_e32 v133, 0x3fb8aa3b, v133
	v_exp_f32_e32 v185, v133
	v_add_f32_e32 v133, 1.0, v152
	v_add_f32_e32 v152, v12, v193
	v_log_f32_e32 v133, v133
	v_mul_f32_e64 v153, |v152|, s19
	v_exp_f32_e32 v153, v153
	v_max_f32_e64 v147, -v147, 0
	v_fmac_f32_e32 v147, 0x3f317218, v133
	v_sub_f32_e32 v133, -0.5, v147
	v_add_f32_e32 v147, 1.0, v153
	v_log_f32_e32 v147, v147
	v_mul_f32_e32 v133, 0x3fb8aa3b, v133
	v_exp_f32_e32 v186, v133
	v_max_f32_e64 v133, -v152, 0
	v_fmac_f32_e32 v133, 0x3f317218, v147
	v_sub_f32_e32 v133, -0.5, v133
	v_mul_f32_e32 v133, 0x3fb8aa3b, v133
	v_exp_f32_e32 v187, v133
	v_add_f32_e32 v133, v13, v194
	v_mul_f32_e64 v147, |v133|, s19
	v_exp_f32_e32 v147, v147
	v_add_f32_e32 v152, v5, v202
	v_mul_f32_e32 v146, 0xbfb8aa3b, v146
	v_mul_f32_e32 v152, 0xbfb8aa3b, v152
	v_add_f32_e32 v147, 1.0, v147
	v_exp_f32_e32 v146, v146
	v_log_f32_e32 v147, v147
	v_exp_f32_e32 v152, v152
	v_max_f32_e64 v133, -v133, 0
	v_add_f32_e32 v146, 1.0, v146
	v_fmac_f32_e32 v133, 0x3f317218, v147
	v_add_f32_e32 v147, 1.0, v152
	v_rcp_f32_e32 v146, v146
	v_rcp_f32_e32 v147, v147
	v_add_f32_e64 v136, v136, -v138
	v_add_f32_e64 v137, v137, -v139
	v_sub_f32_e32 v133, -0.5, v133
	v_fma_f32 v136, v40, v136, v138
	v_fma_f32 v137, v41, v137, v139
	v_add_f32_e64 v138, v146, -1.0
	v_add_f32_e64 v139, v147, -1.0
	v_mul_f32_e32 v133, 0x3fb8aa3b, v133
	v_fma_f32 v138, v48, v138, 1.0
	v_fma_f32 v139, v49, v139, 1.0
	v_exp_f32_e32 v188, v133
	v_mul_f32_e32 v138, v138, v136
	v_mul_f32_e32 v139, v139, v137
	v_mul_f32_e32 v144, v52, v144
	v_mul_f32_e32 v145, v53, v145
	v_cvt_pk_f16_f32 v133, v138, v139
	v_mul_f32_e32 v138, v50, v142
	v_mul_f32_e32 v139, v51, v143
	v_mul_f32_e32 v152, v144, v144
	v_mul_f32_e32 v153, v145, v145
	v_mul_f32_e32 v142, v138, v138
	v_mul_f32_e32 v143, v139, v139
	v_fma_mixlo_f16 v123, v28, v123, v162
	v_add_f32_e32 v142, v142, v143
	v_fma_mixlo_f16 v124, v34, v124, v163
	v_mul_f32_e32 v162, v42, v134
	v_mul_f32_e32 v163, v43, v135
	v_add_f32_e32 v142, v152, v142
	v_cndmask_b32_e64 v164, v164, 0, s[22:23]
	v_mul_f32_e32 v134, v162, v162
	v_mul_f32_e32 v135, v163, v163
	v_add_f32_e32 v142, v153, v142
	v_fma_mixlo_f16 v126, v22, v126, v161
	v_sub_f32_e32 v161, v164, v166
	v_mul_f32_e32 v164, v44, v136
	v_mul_f32_e32 v165, v45, v137
	v_add_f32_e32 v134, v134, v142
	v_mul_f32_e32 v136, v164, v164
	v_mul_f32_e32 v137, v165, v165
	v_add_f32_e32 v134, v135, v134
	v_add_f32_e32 v134, v136, v134
	v_add_f32_e32 v134, v137, v134
	s_ashr_i32 s13, s12, 31
	s_lshl_b64 s[12:13], s[12:13], 11
	v_add_f32_dpp v134, v134, v134 quad_perm:[1,0,3,2] row_mask:0xf bank_mask:0xf bound_ctrl:1
	v_cndmask_b32_e64 v174, v174, 0, s[22:23]
	v_sub_f32_e32 v174, v174, v167
	v_add_f32_dpp v134, v134, v134 quad_perm:[2,3,0,1] row_mask:0xf bank_mask:0xf bound_ctrl:1
	v_sub_f32_e32 v177, v177, v169
	v_sub_f32_e32 v178, v178, v173
	v_add_f32_dpp v134, v134, v134 row_half_mirror row_mask:0xf bank_mask:0xf bound_ctrl:1
	v_rsq_f32_e32 v135, v134
	v_cmp_lt_f32_e32 vcc, s20, v134
	v_fma_mixhi_f16 v129, v17, v177, v169
	v_fma_mixhi_f16 v128, v15, v175, v168
	v_cndmask_b32_e32 v142, v160, v135, vcc
	v_mul_f32_e32 v152, v138, v142
	v_mul_f32_e32 v153, v139, v142
	v_mul_f32_e32 v138, v144, v142
	v_mul_f32_e32 v139, v145, v142
	v_mul_f32_e32 v134, v140, v152
	v_mul_f32_e32 v135, v141, v153
	v_mul_f32_e32 v136, v148, v138
	v_mul_f32_e32 v137, v149, v139
	v_mul_f32_e32 v144, v162, v142
	v_mul_f32_e32 v145, v163, v142
	v_mul_f32_e32 v140, v164, v142
	v_mul_f32_e32 v141, v165, v142
	v_cvt_pk_f16_f32 v134, v134, v135
	v_cvt_pk_f16_f32 v135, v136, v137
	v_mul_f32_e32 v136, v150, v144
	v_mul_f32_e32 v137, v151, v145
	v_mul_f32_e32 v142, v146, v140
	v_mul_f32_e32 v143, v147, v141
	v_lshl_or_b32 v146, v1, 1, s12
	v_mov_b32_e32 v147, s13
	v_cvt_pk_f16_f32 v136, v136, v137
	v_cvt_pk_f16_f32 v137, v142, v143
	v_cvt_pk_f16_f32 v141, v140, v141
	v_cvt_pk_f16_f32 v140, v144, v145
	v_cvt_pk_f16_f32 v145, -v187, -v188
	v_cvt_pk_f16_f32 v144, -v185, -v186
	v_cvt_pk_f16_f32 v143, -v183, -v184
	v_cvt_pk_f16_f32 v142, -v176, -v182
	v_lshl_add_u64 v[148:149], s[0:1], 0, v[146:147]
	v_cvt_pk_f16_f32 v139, v138, v139
	v_cvt_pk_f16_f32 v138, v152, v153
	global_store_dwordx4 v[148:149], v[142:145], off
	v_fma_mixhi_f16 v127, v25, v174, v167
	v_fma_mixhi_f16 v126, v23, v161, v166
	v_lshl_add_u64 v[142:143], s[2:3], 0, v[146:147]
	global_store_dwordx4 v[142:143], v[138:141], off
	s_add_i32 s13, s16, s21
	v_fma_mixhi_f16 v125, v37, v178, v173
	v_lshl_add_u64 v[138:139], s[4:5], 0, v[146:147]
	global_store_dwordx4 v[138:139], v[134:137], off
	v_fma_mixhi_f16 v124, v35, v181, v172
	v_fma_mixhi_f16 v123, v29, v180, v171
	v_lshl_add_u64 v[134:135], s[6:7], 0, v[146:147]
	global_store_dwordx4 v[134:135], v[130:133], off
	v_fma_mixhi_f16 v122, v27, v179, v170
	s_cmp_gt_i32 s13, 0xffff
	v_lshl_add_u64 v[130:131], s[8:9], 0, v[146:147]
	global_store_dwordx4 v[130:131], v[126:129], off
	s_nop 1
	v_lshl_add_u64 v[126:127], s[10:11], 0, v[146:147]
	global_store_dwordx4 v[126:127], v[122:125], off
	s_cbranch_scc1 .LBB0_1222
	s_add_i32 s12, s17, s21
	v_mov_b32_e32 v124, v116
	v_mov_b32_e32 v125, v117
	v_mov_b32_e32 v128, v100
	v_mov_b32_e32 v129, v101
	v_mov_b32_e32 v132, v120
	v_mov_b32_e32 v133, v121
	v_mov_b32_e32 v136, v112
	v_mov_b32_e32 v137, v113
	v_mov_b32_e32 v140, v108
	v_mov_b32_e32 v141, v109
	v_mov_b32_e32 v144, v96
	v_mov_b32_e32 v145, v97
	v_mov_b32_e32 v148, v104
	v_mov_b32_e32 v149, v105
	v_mov_b32_e32 v152, v92
	v_mov_b32_e32 v153, v93
	s_cmp_gt_i32 s12, 0xffff
	v_mov_b32_e32 v122, v114
	v_mov_b32_e32 v123, v115
	v_mov_b32_e32 v126, v98
	v_mov_b32_e32 v127, v99
	v_mov_b32_e32 v130, v118
	v_mov_b32_e32 v131, v119
	v_mov_b32_e32 v134, v110
	v_mov_b32_e32 v135, v111
	v_mov_b32_e32 v138, v106
	v_mov_b32_e32 v139, v107
	v_mov_b32_e32 v142, v94
	v_mov_b32_e32 v143, v95
	v_mov_b32_e32 v146, v102
	v_mov_b32_e32 v147, v103
	v_mov_b32_e32 v150, v90
	v_mov_b32_e32 v151, v91
	s_cbranch_scc1 .LBB0_1221
	s_ashr_i32 s24, s12, 1
	s_and_b32 s12, s12, 0x3ffe
	v_mad_i64_i32 v[122:123], s[22:23], s24, v158, v[154:155]
	s_cmp_eq_u32 s12, 0
	s_cselect_b32 s23, 0, -1
	s_cselect_b32 s22, 0, 0xffffde00
	v_add_co_u32_e32 v124, vcc, 0x1000, v122
	v_lshl_add_u64 v[138:139], v[122:123], 0, s[22:23]
	s_nop 0
	v_addc_co_u32_e32 v125, vcc, 0, v123, vcc
	global_load_dwordx4 v[126:129], v[124:125], off offset:512
	global_load_dwordx4 v[130:133], v[124:125], off offset:2560
	s_nop 0
	global_load_dwordx4 v[122:125], v[122:123], off offset:2560
	s_nop 0
	global_load_dwordx4 v[134:137], v[138:139], off offset:2560
	v_add_co_u32_e32 v142, vcc, 0x1000, v138
	v_mad_i64_i32 v[150:151], s[22:23], s24, v159, v[156:157]
	s_nop 0
	v_addc_co_u32_e32 v143, vcc, 0, v139, vcc
	global_load_dwordx4 v[138:141], v[142:143], off offset:512
	s_nop 0
	global_load_dwordx4 v[142:145], v[142:143], off offset:2560
	s_nop 0
	global_load_dwordx4 v[146:149], v[150:151], off
	s_nop 0
	global_load_dwordx4 v[150:153], v[150:151], off offset:2048
	s_branch .LBB0_1221

.LBB0_1757:
	s_mov_b64 s[0:1], s[54:55]
	s_load_dword s0, s[0:1], 0x138
	s_cmpk_lg_i32 s92, 0x100
	s_cselect_b64 s[12:13], -1, 0
	s_ashr_i32 s34, s93, 3
	s_waitcnt lgkmcnt(0)
	s_cmp_gt_i32 s0, 12
	s_cbranch_scc1 .LBB0_1869
	s_mov_b64 s[0:1], s[54:55]
	s_load_dword s0, s[0:1], 0x13c
	s_waitcnt lgkmcnt(0)
	s_cmp_lt_i32 s0, 13
	s_cbranch_scc1 .LBB0_1869
	s_mov_b64 s[0:1], s[54:55]
	s_load_dwordx2 s[14:15], s[0:1], 0x130
	s_waitcnt vmcnt(0)
	v_mov_b32_e32 v2, v0
	s_movk_i32 s0, 0x104
	s_waitcnt lgkmcnt(0)
	v_readfirstlane_b32 s10, v2
	v_cmp_gt_i32_e32 vcc, s0, v2
	s_barrier
	s_and_saveexec_b64 s[0:1], vcc
	s_cbranch_execz .LBB0_1772
	v_max_i32_e32 v1, 0xffffff04, v2
	v_sub_u32_e32 v1, v1, v2
	s_movk_i32 s2, 0x1ff
	v_add_u32_e32 v1, 0x1ff, v1
	v_cmp_lt_u32_e32 vcc, s2, v1
	s_mov_b64 s[4:5], -1
	v_mov_b32_e32 v4, v2
	s_and_saveexec_b64 s[2:3], vcc
	s_cbranch_execz .LBB0_1769
	v_lshrrev_b32_e32 v1, 9, v1
	v_add_u32_e32 v4, -1, v1
	s_add_u32 s4, s14, 0x10000
	v_add_u32_e32 v3, 0x200, v2
	v_lshrrev_b32_e32 v5, 1, v4
	s_addc_u32 s5, s15, 0
	v_add_u32_e32 v6, 1, v5
	v_cmp_lt_u32_e32 vcc, 5, v4
	v_mov_b32_e32 v4, v2
	v_mov_b32_e32 v5, v3
	s_and_saveexec_b64 s[6:7], vcc
	s_cbranch_execz .LBB0_1765
	v_and_b32_e32 v7, -4, v6
	s_mov_b64 s[8:9], 0
	v_mov_b32_e32 v8, 0x2000
	s_mov_b32 s11, 0x7e07e07f
	s_add_i32 s16, 0, 0x20000
	v_mov_b32_e32 v4, v2
	v_mov_b32_e32 v5, v3

.LBB0_2013:
	s_ashr_i32 s5, s4, 31
	s_lshl_b64 s[16:17], s[4:5], 13
	s_add_u32 s16, s0, s16
	s_addc_u32 s17, s1, s17
	s_add_u32 s20, s16, 0x1000
	s_addc_u32 s21, s17, 0
	global_load_dwordx4 v[16:19], v2, s[20:21]
	global_load_dwordx4 v[20:23], v10, s[20:21]
	global_load_dwordx4 v[60:63], v12, s[20:21]
	global_load_dwordx4 v[64:67], v14, s[20:21]
	s_add_u32 s19, s4, 0x10010
	s_mov_b64 s[16:17], 0
	v_lshl_add_u64 v[50:51], s[20:21], 0, v[2:3]
	v_lshl_add_u64 v[44:45], s[20:21], 0, v[10:11]
	v_lshl_add_u64 v[38:39], s[20:21], 0, v[12:13]
	v_lshl_add_u64 v[32:33], s[20:21], 0, v[14:15]
	s_addc_u32 s20, s5, 0
	v_mov_b32_e32 v56, v8
	v_mov_b32_e32 v57, v9
	s_waitcnt vmcnt(3)
	v_and_b32_e32 v55, 0xffff0000, v16
	v_lshlrev_b32_e32 v54, 16, v16
	v_and_b32_e32 v53, 0xffff0000, v17
	v_lshlrev_b32_e32 v52, 16, v17
	v_and_b32_e32 v49, 0xffff0000, v18
	v_lshlrev_b32_e32 v48, 16, v18
	v_and_b32_e32 v47, 0xffff0000, v19
	v_lshlrev_b32_e32 v46, 16, v19
	s_waitcnt vmcnt(2)
	v_and_b32_e32 v43, 0xffff0000, v20
	v_lshlrev_b32_e32 v42, 16, v20
	v_and_b32_e32 v41, 0xffff0000, v21
	v_lshlrev_b32_e32 v40, 16, v21
	v_and_b32_e32 v37, 0xffff0000, v22
	v_lshlrev_b32_e32 v36, 16, v22
	v_and_b32_e32 v35, 0xffff0000, v23
	v_lshlrev_b32_e32 v34, 16, v23
	s_waitcnt vmcnt(1)
	v_and_b32_e32 v31, 0xffff0000, v60
	v_lshlrev_b32_e32 v30, 16, v60
	v_and_b32_e32 v29, 0xffff0000, v61
	v_lshlrev_b32_e32 v28, 16, v61
	v_and_b32_e32 v27, 0xffff0000, v62
	v_lshlrev_b32_e32 v26, 16, v62
	v_and_b32_e32 v25, 0xffff0000, v63
	v_lshlrev_b32_e32 v24, 16, v63
	s_waitcnt vmcnt(0)
	v_and_b32_e32 v23, 0xffff0000, v64
	v_lshlrev_b32_e32 v22, 16, v64
	v_and_b32_e32 v21, 0xffff0000, v65
	v_lshlrev_b32_e32 v20, 16, v65
	v_and_b32_e32 v19, 0xffff0000, v66
	v_lshlrev_b32_e32 v18, 16, v66
	v_and_b32_e32 v17, 0xffff0000, v67
	v_lshlrev_b32_e32 v16, 16, v67

.LBB0_2137:
	s_add_i32 s16, s4, 0x2000
	s_ashr_i32 s17, s16, 31
	s_lshl_b64 s[18:19], s[16:17], 13
	s_add_u32 s18, s0, s18
	s_addc_u32 s19, s1, s19
	s_add_u32 s20, s18, 0x1000
	s_addc_u32 s21, s19, 0
	global_load_dwordx4 v[16:19], v2, s[20:21]
	global_load_dwordx4 v[20:23], v10, s[20:21]
	global_load_dwordx4 v[60:63], v12, s[20:21]
	global_load_dwordx4 v[64:67], v14, s[20:21]
	s_ashr_i32 s22, s4, 31
	v_lshl_add_u64 v[50:51], s[20:21], 0, v[2:3]
	v_lshl_add_u64 v[44:45], s[20:21], 0, v[10:11]
	v_lshl_add_u64 v[38:39], s[20:21], 0, v[12:13]
	v_lshl_add_u64 v[32:33], s[20:21], 0, v[14:15]
	s_add_u32 s20, s4, 0x10010
	s_mov_b64 s[18:19], 0
	s_addc_u32 s21, s22, 0
	v_mov_b32_e32 v56, v8
	v_mov_b32_e32 v57, v9
	s_waitcnt vmcnt(3)
	v_and_b32_e32 v55, 0xffff0000, v16
	v_lshlrev_b32_e32 v54, 16, v16
	v_and_b32_e32 v53, 0xffff0000, v17
	v_lshlrev_b32_e32 v52, 16, v17
	v_and_b32_e32 v49, 0xffff0000, v18
	v_lshlrev_b32_e32 v48, 16, v18
	v_and_b32_e32 v47, 0xffff0000, v19
	v_lshlrev_b32_e32 v46, 16, v19
	s_waitcnt vmcnt(2)
	v_and_b32_e32 v43, 0xffff0000, v20
	v_lshlrev_b32_e32 v42, 16, v20
	v_and_b32_e32 v41, 0xffff0000, v21
	v_lshlrev_b32_e32 v40, 16, v21
	v_and_b32_e32 v37, 0xffff0000, v22
	v_lshlrev_b32_e32 v36, 16, v22
	v_and_b32_e32 v35, 0xffff0000, v23
	v_lshlrev_b32_e32 v34, 16, v23
	s_waitcnt vmcnt(1)
	v_and_b32_e32 v31, 0xffff0000, v60
	v_lshlrev_b32_e32 v30, 16, v60
	v_and_b32_e32 v29, 0xffff0000, v61
	v_lshlrev_b32_e32 v28, 16, v61
	v_and_b32_e32 v27, 0xffff0000, v62
	v_lshlrev_b32_e32 v26, 16, v62
	v_and_b32_e32 v25, 0xffff0000, v63
	v_lshlrev_b32_e32 v24, 16, v63
	s_waitcnt vmcnt(0)
	v_and_b32_e32 v23, 0xffff0000, v64
	v_lshlrev_b32_e32 v22, 16, v64
	v_and_b32_e32 v21, 0xffff0000, v65
	v_lshlrev_b32_e32 v20, 16, v65
	v_and_b32_e32 v19, 0xffff0000, v66
	v_lshlrev_b32_e32 v18, 16, v66
	v_and_b32_e32 v17, 0xffff0000, v67
	v_lshlrev_b32_e32 v16, 16, v67

.LBB0_2261:
	s_add_i32 s16, s4, 0x4000
	s_ashr_i32 s17, s16, 31
	s_lshl_b64 s[18:19], s[16:17], 13
	s_add_u32 s18, s0, s18
	s_addc_u32 s19, s1, s19
	s_add_u32 s20, s18, 0x1000
	s_addc_u32 s21, s19, 0
	global_load_dwordx4 v[16:19], v2, s[20:21]
	global_load_dwordx4 v[20:23], v10, s[20:21]
	global_load_dwordx4 v[60:63], v12, s[20:21]
	global_load_dwordx4 v[64:67], v14, s[20:21]
	s_ashr_i32 s22, s4, 31
	v_lshl_add_u64 v[50:51], s[20:21], 0, v[2:3]
	v_lshl_add_u64 v[44:45], s[20:21], 0, v[10:11]
	v_lshl_add_u64 v[38:39], s[20:21], 0, v[12:13]
	v_lshl_add_u64 v[32:33], s[20:21], 0, v[14:15]
	s_add_u32 s20, s4, 0x10010
	s_mov_b64 s[18:19], 0
	s_addc_u32 s21, s22, 0
	v_mov_b32_e32 v56, v8
	v_mov_b32_e32 v57, v9
	s_waitcnt vmcnt(3)
	v_and_b32_e32 v55, 0xffff0000, v16
	v_lshlrev_b32_e32 v54, 16, v16
	v_and_b32_e32 v53, 0xffff0000, v17
	v_lshlrev_b32_e32 v52, 16, v17
	v_and_b32_e32 v49, 0xffff0000, v18
	v_lshlrev_b32_e32 v48, 16, v18
	v_and_b32_e32 v47, 0xffff0000, v19
	v_lshlrev_b32_e32 v46, 16, v19
	s_waitcnt vmcnt(2)
	v_and_b32_e32 v43, 0xffff0000, v20
	v_lshlrev_b32_e32 v42, 16, v20
	v_and_b32_e32 v41, 0xffff0000, v21
	v_lshlrev_b32_e32 v40, 16, v21
	v_and_b32_e32 v37, 0xffff0000, v22
	v_lshlrev_b32_e32 v36, 16, v22
	v_and_b32_e32 v35, 0xffff0000, v23
	v_lshlrev_b32_e32 v34, 16, v23
	s_waitcnt vmcnt(1)
	v_and_b32_e32 v31, 0xffff0000, v60
	v_lshlrev_b32_e32 v30, 16, v60
	v_and_b32_e32 v29, 0xffff0000, v61
	v_lshlrev_b32_e32 v28, 16, v61
	v_and_b32_e32 v27, 0xffff0000, v62
	v_lshlrev_b32_e32 v26, 16, v62
	v_and_b32_e32 v25, 0xffff0000, v63
	v_lshlrev_b32_e32 v24, 16, v63
	s_waitcnt vmcnt(0)
	v_and_b32_e32 v23, 0xffff0000, v64
	v_lshlrev_b32_e32 v22, 16, v64
	v_and_b32_e32 v21, 0xffff0000, v65
	v_lshlrev_b32_e32 v20, 16, v65
	v_and_b32_e32 v19, 0xffff0000, v66
	v_lshlrev_b32_e32 v18, 16, v66
	v_and_b32_e32 v17, 0xffff0000, v67
	v_lshlrev_b32_e32 v16, 16, v67

.LBB0_2322:
	s_add_i32 s14, s4, 0x4000
	s_ashr_i32 s15, s14, 31
	s_lshl_b64 s[16:17], s[14:15], 13
	s_add_u32 s16, s0, s16
	s_addc_u32 s17, s1, s17
	s_add_u32 s18, s16, 0x1000
	s_addc_u32 s19, s17, 0
	global_load_dwordx4 v[16:19], v2, s[18:19]
	global_load_dwordx4 v[20:23], v10, s[18:19]
	global_load_dwordx4 v[60:63], v12, s[18:19]
	global_load_dwordx4 v[64:67], v14, s[18:19]
	s_ashr_i32 s20, s4, 31
	v_lshl_add_u64 v[50:51], s[18:19], 0, v[2:3]
	v_lshl_add_u64 v[44:45], s[18:19], 0, v[10:11]
	v_lshl_add_u64 v[38:39], s[18:19], 0, v[12:13]
	v_lshl_add_u64 v[32:33], s[18:19], 0, v[14:15]
	s_add_u32 s18, s4, 0x10010
	s_mov_b64 s[16:17], 0
	s_addc_u32 s19, s20, 0
	v_mov_b32_e32 v56, v8
	v_mov_b32_e32 v57, v9
	s_waitcnt vmcnt(3)
	v_and_b32_e32 v55, 0xffff0000, v16
	v_lshlrev_b32_e32 v54, 16, v16
	v_and_b32_e32 v53, 0xffff0000, v17
	v_lshlrev_b32_e32 v52, 16, v17
	v_and_b32_e32 v49, 0xffff0000, v18
	v_lshlrev_b32_e32 v48, 16, v18
	v_and_b32_e32 v47, 0xffff0000, v19
	v_lshlrev_b32_e32 v46, 16, v19
	s_waitcnt vmcnt(2)
	v_and_b32_e32 v43, 0xffff0000, v20
	v_lshlrev_b32_e32 v42, 16, v20
	v_and_b32_e32 v41, 0xffff0000, v21
	v_lshlrev_b32_e32 v40, 16, v21
	v_and_b32_e32 v37, 0xffff0000, v22
	v_lshlrev_b32_e32 v36, 16, v22
	v_and_b32_e32 v35, 0xffff0000, v23
	v_lshlrev_b32_e32 v34, 16, v23
	s_waitcnt vmcnt(1)
	v_and_b32_e32 v31, 0xffff0000, v60
	v_lshlrev_b32_e32 v30, 16, v60
	v_and_b32_e32 v29, 0xffff0000, v61
	v_lshlrev_b32_e32 v28, 16, v61
	v_and_b32_e32 v27, 0xffff0000, v62
	v_lshlrev_b32_e32 v26, 16, v62
	v_and_b32_e32 v25, 0xffff0000, v63
	v_lshlrev_b32_e32 v24, 16, v63
	s_waitcnt vmcnt(0)
	v_and_b32_e32 v23, 0xffff0000, v64
	v_lshlrev_b32_e32 v22, 16, v64
	v_and_b32_e32 v21, 0xffff0000, v65
	v_lshlrev_b32_e32 v20, 16, v65
	v_and_b32_e32 v19, 0xffff0000, v66
	v_lshlrev_b32_e32 v18, 16, v66
	v_and_b32_e32 v17, 0xffff0000, v67
	v_lshlrev_b32_e32 v16, 16, v67

.LBB0_2385:
	s_add_i32 s14, s4, 0x6000
	s_ashr_i32 s15, s14, 31
	s_lshl_b64 s[16:17], s[14:15], 13
	s_add_u32 s16, s0, s16
	s_addc_u32 s17, s1, s17
	s_add_u32 s18, s16, 0x1000
	s_addc_u32 s19, s17, 0
	global_load_dwordx4 v[16:19], v2, s[18:19]
	global_load_dwordx4 v[20:23], v10, s[18:19]
	global_load_dwordx4 v[60:63], v12, s[18:19]
	global_load_dwordx4 v[64:67], v14, s[18:19]
	s_ashr_i32 s20, s4, 31
	v_lshl_add_u64 v[50:51], s[18:19], 0, v[2:3]
	v_lshl_add_u64 v[44:45], s[18:19], 0, v[10:11]
	v_lshl_add_u64 v[38:39], s[18:19], 0, v[12:13]
	v_lshl_add_u64 v[32:33], s[18:19], 0, v[14:15]
	s_add_u32 s18, s4, 0x10010
	s_mov_b64 s[16:17], 0
	s_addc_u32 s19, s20, 0
	v_mov_b32_e32 v56, v8
	v_mov_b32_e32 v57, v9
	s_waitcnt vmcnt(3)
	v_and_b32_e32 v55, 0xffff0000, v16
	v_lshlrev_b32_e32 v54, 16, v16
	v_and_b32_e32 v53, 0xffff0000, v17
	v_lshlrev_b32_e32 v52, 16, v17
	v_and_b32_e32 v49, 0xffff0000, v18
	v_lshlrev_b32_e32 v48, 16, v18
	v_and_b32_e32 v47, 0xffff0000, v19
	v_lshlrev_b32_e32 v46, 16, v19
	s_waitcnt vmcnt(2)
	v_and_b32_e32 v43, 0xffff0000, v20
	v_lshlrev_b32_e32 v42, 16, v20
	v_and_b32_e32 v41, 0xffff0000, v21
	v_lshlrev_b32_e32 v40, 16, v21
	v_and_b32_e32 v37, 0xffff0000, v22
	v_lshlrev_b32_e32 v36, 16, v22
	v_and_b32_e32 v35, 0xffff0000, v23
	v_lshlrev_b32_e32 v34, 16, v23
	s_waitcnt vmcnt(1)
	v_and_b32_e32 v31, 0xffff0000, v60
	v_lshlrev_b32_e32 v30, 16, v60
	v_and_b32_e32 v29, 0xffff0000, v61
	v_lshlrev_b32_e32 v28, 16, v61
	v_and_b32_e32 v27, 0xffff0000, v62
	v_lshlrev_b32_e32 v26, 16, v62
	v_and_b32_e32 v25, 0xffff0000, v63
	v_lshlrev_b32_e32 v24, 16, v63
	s_waitcnt vmcnt(0)
	v_and_b32_e32 v23, 0xffff0000, v64
	v_lshlrev_b32_e32 v22, 16, v64
	v_and_b32_e32 v21, 0xffff0000, v65
	v_lshlrev_b32_e32 v20, 16, v65
	v_and_b32_e32 v19, 0xffff0000, v66
	v_lshlrev_b32_e32 v18, 16, v66
	v_and_b32_e32 v17, 0xffff0000, v67
	v_lshlrev_b32_e32 v16, 16, v67
